# P0: g_mix gains hoisted out of the XN row loop (removes 4 vmcnt(0) drains per row that killed the next-row prefetch); S5: lag-table loads batched, MOUT fragment loads software-pipelined through 8 regi
# speedup vs baseline: 1.4113x; 1.0049x over previous
.LBB0_35:
	s_or_b64 exec, exec, s[0:1]
	v_and_b32_e32 v96, 63, v2
	s_ashr_i32 s0, s26, 6
	v_readlane_b32 s1, v255, 16
	v_lshlrev_b32_e32 v1, 3, v96
	s_add_i32 s0, s0, s1
	v_or_b32_e32 v2, 0x400, v1
	v_or_b32_e32 v3, 0x600, v1
	s_cmpk_lt_i32 s0, 0x4000
	v_lshlrev_b32_e32 v74, 2, v3
	v_lshlrev_b32_e32 v100, 2, v2
	v_lshlrev_b32_e32 v102, 2, v1
	v_mbcnt_hi_u32_b32 v1, -1, v117
	v_lshlrev_b32_e32 v98, 4, v96
	s_waitcnt lgkmcnt(0)
	s_barrier
	s_cbranch_scc0 .LBB0_40
	s_load_dwordx2 s[44:45], s[30:31], 0x0
	s_load_dwordx2 s[4:5], s[30:31], 0x10
	s_ashr_i32 s1, s0, 31
	s_lshl_b64 s[6:7], s[0:1], 13
	v_and_b32_e32 v2, 64, v1
	s_waitcnt lgkmcnt(0)
	s_add_u32 s6, s44, s6
	s_addc_u32 s7, s45, s7
	global_load_dwordx4 v[34:37], v74, s[6:7] offset:16
	global_load_dwordx4 v[38:41], v74, s[6:7]
	global_load_dwordx4 v[42:45], v100, s[6:7] offset:16
	global_load_dwordx4 v[46:49], v100, s[6:7]
	global_load_dwordx4 v[50:53], v102, s[6:7] offset:2064
	global_load_dwordx4 v[54:57], v102, s[6:7] offset:2048
	global_load_dwordx4 v[58:61], v102, s[6:7] offset:16
	global_load_dwordx4 v[62:65], v102, s[6:7]
	v_add_u32_e32 v2, 64, v2
	v_xor_b32_e32 v3, 1, v1
	v_cmp_lt_i32_e32 vcc, v3, v2
	s_lshl_b64 s[20:21], s[0:1], 5
	s_add_u32 s20, s20, 0x5d30000
	v_cndmask_b32_e32 v3, v1, v3, vcc
	v_lshlrev_b32_e32 v95, 2, v3
	v_xor_b32_e32 v3, 2, v1
	v_cmp_lt_i32_e32 vcc, v3, v2
	s_addc_u32 s21, s21, 0
	v_mov_b32_e32 v101, v75
	v_cndmask_b32_e32 v3, v1, v3, vcc
	v_lshlrev_b32_e32 v99, 2, v3
	v_xor_b32_e32 v3, 4, v1
	v_cmp_lt_i32_e32 vcc, v3, v2
	v_mov_b32_e32 v103, v75
	v_lshl_add_u32 v4, v96, 8, 0
	v_cndmask_b32_e32 v3, v1, v3, vcc
	v_lshlrev_b32_e32 v122, 2, v3
	v_xor_b32_e32 v3, 8, v1
	v_cmp_lt_i32_e32 vcc, v3, v2
	v_cmp_gt_u32_e64 s[18:19], 8, v96
	v_lshl_add_u64 v[104:105], s[4:5], 0, v[102:103]
	v_cndmask_b32_e32 v3, v1, v3, vcc
	v_lshlrev_b32_e32 v123, 2, v3
	v_xor_b32_e32 v3, 16, v1
	v_cmp_lt_i32_e32 vcc, v3, v2
	v_lshl_add_u64 v[106:107], s[4:5], 0, v[100:101]
	v_lshl_add_u64 v[108:109], s[4:5], 0, v[74:75]
	v_cndmask_b32_e32 v3, v1, v3, vcc
	v_lshlrev_b32_e32 v124, 2, v3
	v_xor_b32_e32 v3, 32, v1
	v_cmp_lt_i32_e32 vcc, v3, v2
	v_cmp_eq_u32_e64 s[4:5], 1, v96
	v_cmp_eq_u32_e64 s[6:7], 2, v96
	v_cndmask_b32_e32 v2, v1, v3, vcc
	v_lshlrev_b32_e32 v125, 2, v2
	v_or_b32_e32 v2, 64, v96
	v_lshl_add_u32 v5, v2, 8, 0
	v_lshlrev_b32_e32 v6, 4, v2
	v_or_b32_e32 v2, 0x80, v96
	v_lshl_add_u32 v7, v2, 8, 0
	v_lshlrev_b32_e32 v8, 4, v2
	v_or_b32_e32 v2, 0xc0, v96
	v_lshl_add_u32 v9, v2, 8, 0
	v_lshlrev_b32_e32 v10, 4, v2
	v_lshlrev_b32_e32 v2, 2, v96
	v_mov_b32_e32 v3, v75
	v_lshl_add_u64 v[110:111], s[20:21], 0, v[2:3]
	s_lshl_b64 s[20:21], s[0:1], 12
	v_cmp_eq_u32_e64 s[8:9], 3, v96
	v_cmp_eq_u32_e64 s[10:11], 4, v96
	v_cmp_eq_u32_e64 s[12:13], 5, v96
	v_cmp_eq_u32_e64 s[14:15], 6, v96
	v_cmp_eq_u32_e64 s[16:17], 7, v96
	v_or_b32_e32 v112, s20, v98
	v_mov_b32_e32 v113, s21
	v_add_u32_e32 v101, v4, v98
	v_add_u32_e32 v103, v5, v6
	v_add_u32_e32 v126, v7, v8
	v_add_u32_e32 v127, v9, v10
	v_lshlrev_b32_e32 v128, 2, v96
	s_mov_b32 s1, s0
	global_load_dwordx4 v[200:203], v[104:105], off
	global_load_dwordx4 v[204:207], v[104:105], off offset:16
	global_load_dwordx4 v[208:211], v[104:105], off offset:2048
	global_load_dwordx4 v[212:215], v[104:105], off offset:2064
	global_load_dwordx4 v[216:219], v[106:107], off
	global_load_dwordx4 v[220:223], v[106:107], off offset:16
	global_load_dwordx4 v[224:227], v[108:109], off
	global_load_dwordx4 v[228:231], v[108:109], off offset:16
	s_branch .LBB0_38
.LBB0_37:
	s_or_b64 exec, exec, s[20:21]
	s_waitcnt vmcnt(0)
	v_mov_b64_e32 v[36:37], v[28:29]
	s_waitcnt lgkmcnt(4)
	v_mov_b64_e32 v[40:41], v[32:33]
	s_waitcnt lgkmcnt(2)
	v_mov_b64_e32 v[44:45], v[20:21]
	s_waitcnt lgkmcnt(0)
	v_mov_b64_e32 v[48:49], v[24:25]
	v_mov_b64_e32 v[52:53], v[12:13]
	v_mov_b64_e32 v[56:57], v[16:17]
	v_mov_b64_e32 v[60:61], v[4:5]
	v_mov_b64_e32 v[64:65], v[8:9]
	v_lshl_add_u64 v[110:111], v[110:111], 0, s[90:91]
	v_lshl_add_u64 v[112:113], v[112:113], 0, s[92:93]
	s_and_b64 vcc, exec, s[46:47]
	v_mov_b64_e32 v[34:35], v[26:27]
	v_mov_b64_e32 v[38:39], v[30:31]
	v_mov_b64_e32 v[42:43], v[18:19]
	v_mov_b64_e32 v[46:47], v[22:23]
	v_mov_b64_e32 v[50:51], v[10:11]
	v_mov_b64_e32 v[54:55], v[14:15]
	v_mov_b64_e32 v[58:59], v[2:3]
	v_mov_b64_e32 v[62:63], v[6:7]
	s_cbranch_vccnz .LBB0_40
.LBB0_38:
	s_waitcnt vmcnt(1)
	v_mul_f32_e32 v66, v58, v58
	v_mul_f32_e32 v67, v59, v59
	s_waitcnt vmcnt(0)
	v_fmac_f32_e32 v66, v62, v62
	v_fmac_f32_e32 v67, v63, v63
	v_add_f32_e32 v66, v66, v67
	v_mul_f32_e32 v67, v60, v60
	v_fmac_f32_e32 v67, v64, v64
	v_add_f32_e32 v66, v66, v67
	v_mul_f32_e32 v67, v61, v61
	v_fmac_f32_e32 v67, v65, v65
	v_add_f32_e32 v66, v66, v67
	v_mul_f32_e32 v67, v50, v50
	v_fmac_f32_e32 v67, v54, v54
	v_add_f32_e32 v66, v66, v67
	v_mul_f32_e32 v67, v51, v51
	v_fmac_f32_e32 v67, v55, v55
	v_add_f32_e32 v66, v66, v67
	v_mul_f32_e32 v67, v52, v52
	v_fmac_f32_e32 v67, v56, v56
	v_add_f32_e32 v66, v66, v67
	v_mul_f32_e32 v67, v53, v53
	v_fmac_f32_e32 v67, v57, v57
	v_add_f32_e32 v66, v66, v67
	v_mul_f32_e32 v67, v42, v42
	v_fmac_f32_e32 v67, v46, v46
	v_add_f32_e32 v66, v66, v67
	v_mul_f32_e32 v67, v43, v43
	v_fmac_f32_e32 v67, v47, v47
	v_add_f32_e32 v66, v66, v67
	v_mul_f32_e32 v67, v44, v44
	v_fmac_f32_e32 v67, v48, v48
	v_add_f32_e32 v66, v66, v67
	v_mul_f32_e32 v67, v45, v45
	v_fmac_f32_e32 v67, v49, v49
	v_add_f32_e32 v66, v66, v67
	v_mul_f32_e32 v67, v34, v34
	v_fmac_f32_e32 v67, v38, v38
	v_add_f32_e32 v66, v66, v67
	v_mul_f32_e32 v67, v35, v35
	v_fmac_f32_e32 v67, v39, v39
	v_add_f32_e32 v68, v66, v67
	v_pk_mul_f32 v[66:67], v[36:37], v[36:37]
	s_mov_b32 s20, s1
	v_pk_fma_f32 v[66:67], v[40:41], v[40:41], v[66:67]
	s_add_i32 s1, s1, s74
	v_add_f32_e32 v66, v68, v66
	v_add_f32_e32 v66, v66, v67
	ds_bpermute_b32 v67, v95, v66
	s_cmpk_gt_i32 s1, 0x3fff
	s_cselect_b64 s[46:47], -1, 0
	s_cmpk_lt_i32 s1, 0x4000
	s_cselect_b32 s20, s1, s20
	s_waitcnt lgkmcnt(0)
	v_add_f32_e32 v66, v66, v67
	ds_bpermute_b32 v67, v99, v66
	s_ashr_i32 s21, s20, 31
	s_lshl_b64 s[20:21], s[20:21], 13
	s_add_u32 s20, s44, s20
	s_addc_u32 s21, s45, s21
	s_waitcnt lgkmcnt(0)
	v_add_f32_e32 v66, v66, v67
	ds_bpermute_b32 v67, v122, v66
	global_load_dwordx4 v[2:5], v102, s[20:21] offset:16
	global_load_dwordx4 v[6:9], v102, s[20:21]
	global_load_dwordx4 v[10:13], v102, s[20:21] offset:2064
	global_load_dwordx4 v[14:17], v102, s[20:21] offset:2048
	global_load_dwordx4 v[18:21], v100, s[20:21] offset:16
	global_load_dwordx4 v[22:25], v100, s[20:21]
	global_load_dwordx4 v[26:29], v74, s[20:21] offset:16
	global_load_dwordx4 v[30:33], v74, s[20:21]
	s_waitcnt lgkmcnt(0)
	v_add_f32_e32 v66, v66, v67
	ds_bpermute_b32 v67, v123, v66
	s_waitcnt lgkmcnt(0)
	v_add_f32_e32 v66, v66, v67
	ds_bpermute_b32 v67, v124, v66
	s_waitcnt lgkmcnt(0)
	v_add_f32_e32 v66, v66, v67
	ds_bpermute_b32 v67, v125, v66
	s_waitcnt lgkmcnt(0)
	v_add_f32_e32 v66, v66, v67
	v_fmamk_f32 v66, v66, 0x3a000000, v115
	v_cmp_gt_f32_e32 vcc, s80, v66
	v_mul_f32_e32 v67, 0x4f800000, v66
	s_nop 0
	v_cndmask_b32_e32 v66, v66, v67, vcc
	v_sqrt_f32_e32 v67, v66
	s_nop 0
	v_add_u32_e32 v68, -1, v67
	v_fma_f32 v69, -v68, v67, v66
	v_cmp_ge_f32_e64 s[20:21], 0, v69
	v_add_u32_e32 v69, 1, v67
	s_nop 0
	v_cndmask_b32_e64 v68, v67, v68, s[20:21]
	v_fma_f32 v67, -v69, v67, v66
	v_cmp_lt_f32_e64 s[20:21], 0, v67
	s_nop 1
	v_cndmask_b32_e64 v67, v68, v69, s[20:21]
	v_mul_f32_e32 v68, 0x37800000, v67
	v_cndmask_b32_e32 v67, v67, v68, vcc
	v_cmp_class_f32_e32 vcc, v66, v116
	s_nop 1
	v_cndmask_b32_e32 v66, v67, v66, vcc
	v_div_scale_f32 v67, s[20:21], v66, v66, 1.0
	v_rcp_f32_e32 v68, v67
	s_brev_b32 s20, 16
	v_fma_f32 v69, -v67, v68, 1.0
	v_fmac_f32_e32 v68, v69, v68
	v_div_scale_f32 v69, vcc, 1.0, v66, 1.0
	v_mul_f32_e32 v70, v69, v68
	v_fma_f32 v71, -v67, v70, v69
	v_fmac_f32_e32 v70, v71, v68
	v_fma_f32 v67, -v67, v70, v69
	v_div_fmas_f32 v67, v67, v68, v70
	v_div_fixup_f32 v114, v67, v66, 1.0
	v_pk_mul_f32 v[130:131], v[114:115], v[200:201] op_sel_hi:[0,1]
	v_pk_mul_f32 v[70:71], v[114:115], v[202:203] op_sel_hi:[0,1]
	v_pk_mul_f32 v[70:71], v[70:71], v[64:65]
	v_pk_mul_f32 v[142:143], v[130:131], v[62:63]
	v_pk_mul_f32 v[64:65], v[114:115], v[204:205] op_sel_hi:[0,1]
	v_pk_mul_f32 v[62:63], v[114:115], v[206:207] op_sel_hi:[0,1]
	v_lshl_add_u64 v[66:67], s[34:35], 0, v[112:113]
	v_pk_mul_f32 v[62:63], v[62:63], v[60:61]
	v_pk_mul_f32 v[64:65], v[64:65], v[58:59]
	v_add_co_u32_e32 v72, vcc, s20, v66
	v_cvt_pk_f16_f32 v58, v142, v143
	v_cvt_pk_f16_f32 v59, v70, v71
	v_cvt_pk_f16_f32 v60, v64, v65
	v_cvt_pk_f16_f32 v61, v62, v63
	v_addc_co_u32_e32 v73, vcc, 0, v67, vcc
	global_store_dwordx4 v[72:73], v[58:61], off
	s_nop 1
	v_pk_mul_f32 v[130:131], v[114:115], v[208:209] op_sel_hi:[0,1]
	v_pk_mul_f32 v[58:59], v[114:115], v[210:211] op_sel_hi:[0,1]
	v_pk_mul_f32 v[58:59], v[58:59], v[56:57]
	v_pk_mul_f32 v[60:61], v[130:131], v[54:55]
	v_pk_mul_f32 v[56:57], v[114:115], v[212:213] op_sel_hi:[0,1]
	v_pk_mul_f32 v[54:55], v[114:115], v[214:215] op_sel_hi:[0,1]
	v_pk_mul_f32 v[54:55], v[54:55], v[52:53]
	v_pk_mul_f32 v[56:57], v[56:57], v[50:51]
	v_cvt_pk_f16_f32 v50, v60, v61
	v_cvt_pk_f16_f32 v51, v58, v59
	v_cvt_pk_f16_f32 v52, v56, v57
	v_cvt_pk_f16_f32 v53, v54, v55
	global_store_dwordx4 v[72:73], v[50:53], off offset:1024
	s_nop 1
	v_pk_mul_f32 v[130:131], v[114:115], v[216:217] op_sel_hi:[0,1]
	v_pk_mul_f32 v[50:51], v[114:115], v[218:219] op_sel_hi:[0,1]
	v_pk_mul_f32 v[50:51], v[50:51], v[48:49]
	v_pk_mul_f32 v[52:53], v[130:131], v[46:47]
	v_pk_mul_f32 v[48:49], v[114:115], v[220:221] op_sel_hi:[0,1]
	v_pk_mul_f32 v[46:47], v[114:115], v[222:223] op_sel_hi:[0,1]
	v_pk_mul_f32 v[46:47], v[46:47], v[44:45]
	v_pk_mul_f32 v[48:49], v[48:49], v[42:43]
	v_cvt_pk_f16_f32 v42, v52, v53
	v_cvt_pk_f16_f32 v43, v50, v51
	v_cvt_pk_f16_f32 v44, v48, v49
	v_cvt_pk_f16_f32 v45, v46, v47
	global_store_dwordx4 v[72:73], v[42:45], off offset:2048
	s_nop 1
	v_pk_mul_f32 v[130:131], v[114:115], v[224:225] op_sel_hi:[0,1]
	v_pk_mul_f32 v[42:43], v[114:115], v[226:227] op_sel_hi:[0,1]
	v_pk_mul_f32 v[42:43], v[42:43], v[40:41]
	v_pk_mul_f32 v[44:45], v[130:131], v[38:39]
	v_pk_mul_f32 v[40:41], v[114:115], v[228:229] op_sel_hi:[0,1]
	v_pk_mul_f32 v[38:39], v[114:115], v[230:231] op_sel_hi:[0,1]
	v_pk_mul_f32 v[38:39], v[38:39], v[36:37]
	v_pk_mul_f32 v[40:41], v[40:41], v[34:35]
	v_cvt_pk_f16_f32 v34, v44, v45
	v_cvt_pk_f16_f32 v35, v42, v43
	v_cvt_pk_f16_f32 v36, v40, v41
	v_cvt_pk_f16_f32 v37, v38, v39
	global_store_dwordx4 v[72:73], v[34:37], off offset:3072
	ds_read_b128 v[34:37], v101
	ds_read_b128 v[130:133], v101 offset:16
	ds_read_b128 v[134:137], v101 offset:32
	ds_read_b128 v[138:141], v101 offset:48
	s_waitcnt lgkmcnt(3)
	v_fma_f32 v72, v142, v34, 0
	s_waitcnt lgkmcnt(2)
	v_fma_f32 v69, v142, v130, 0
	v_fma_f32 v73, v142, v35, 0
	v_fma_f32 v66, v142, v131, 0
	v_fma_f32 v114, v142, v36, 0
	v_fma_f32 v67, v142, v132, 0
	v_fma_f32 v129, v142, v37, 0
	v_fma_f32 v68, v142, v133, 0
	ds_read_b128 v[34:37], v101 offset:64
	ds_read_b128 v[130:133], v101 offset:80
	s_waitcnt lgkmcnt(3)
	v_fmac_f32_e32 v72, v143, v134
	s_waitcnt lgkmcnt(2)
	v_fmac_f32_e32 v69, v143, v138
	v_fmac_f32_e32 v73, v143, v135
	v_fmac_f32_e32 v66, v143, v139
	v_fmac_f32_e32 v114, v143, v136
	v_fmac_f32_e32 v67, v143, v140
	v_fmac_f32_e32 v129, v143, v137
	v_fmac_f32_e32 v68, v143, v141
	s_waitcnt lgkmcnt(1)
	v_fmac_f32_e32 v72, v70, v34
	s_waitcnt lgkmcnt(0)
	v_fmac_f32_e32 v69, v70, v130
	v_fmac_f32_e32 v73, v70, v35
	v_fmac_f32_e32 v66, v70, v131
	v_fmac_f32_e32 v114, v70, v36
	v_fmac_f32_e32 v67, v70, v132
	v_fmac_f32_e32 v129, v70, v37
	v_fmac_f32_e32 v68, v70, v133
	ds_read_b128 v[34:37], v101 offset:96
	ds_read_b128 v[130:133], v101 offset:112
	s_waitcnt lgkmcnt(1)
	v_fmac_f32_e32 v72, v71, v34
	s_waitcnt lgkmcnt(0)
	v_fmac_f32_e32 v69, v71, v130
	v_fmac_f32_e32 v73, v71, v35
	v_fmac_f32_e32 v66, v71, v131
	v_fmac_f32_e32 v114, v71, v36
	v_fmac_f32_e32 v67, v71, v132
	v_fmac_f32_e32 v129, v71, v37
	v_fmac_f32_e32 v68, v71, v133
	ds_read_b128 v[34:37], v101 offset:128
	ds_read_b128 v[130:133], v101 offset:144
	s_waitcnt lgkmcnt(1)
	v_fmac_f32_e32 v72, v64, v34
	s_waitcnt lgkmcnt(0)
	v_fmac_f32_e32 v69, v64, v130
	v_fmac_f32_e32 v73, v64, v35
	v_fmac_f32_e32 v66, v64, v131
	v_fmac_f32_e32 v114, v64, v36
	v_fmac_f32_e32 v67, v64, v132
	v_fmac_f32_e32 v129, v64, v37
	v_fmac_f32_e32 v68, v64, v133
	ds_read_b128 v[34:37], v101 offset:160
	ds_read_b128 v[130:133], v101 offset:176
	s_waitcnt lgkmcnt(1)
	v_fmac_f32_e32 v72, v65, v34
	s_waitcnt lgkmcnt(0)
	v_fmac_f32_e32 v69, v65, v130
	v_fmac_f32_e32 v73, v65, v35
	v_fmac_f32_e32 v66, v65, v131
	v_fmac_f32_e32 v114, v65, v36
	v_fmac_f32_e32 v67, v65, v132
	v_fmac_f32_e32 v129, v65, v37
	v_fmac_f32_e32 v68, v65, v133
	ds_read_b128 v[34:37], v101 offset:192
	ds_read_b128 v[130:133], v101 offset:208
	s_waitcnt lgkmcnt(1)
	v_fmac_f32_e32 v72, v62, v34
	s_waitcnt lgkmcnt(0)
	v_fmac_f32_e32 v69, v62, v130
	v_fmac_f32_e32 v73, v62, v35
	v_fmac_f32_e32 v66, v62, v131
	v_fmac_f32_e32 v114, v62, v36
	v_fmac_f32_e32 v67, v62, v132
	v_fmac_f32_e32 v129, v62, v37
	v_fmac_f32_e32 v68, v62, v133
	ds_read_b128 v[130:133], v101 offset:224
	ds_read_b128 v[34:37], v101 offset:240
	s_waitcnt lgkmcnt(1)
	v_fmac_f32_e32 v72, v63, v130
	s_waitcnt lgkmcnt(0)
	v_fmac_f32_e32 v69, v63, v34
	v_fmac_f32_e32 v73, v63, v131
	v_fmac_f32_e32 v66, v63, v35
	v_fmac_f32_e32 v114, v63, v132
	v_fmac_f32_e32 v67, v63, v36
	v_fmac_f32_e32 v129, v63, v133
	v_fmac_f32_e32 v68, v63, v37
	ds_read_b128 v[34:37], v103
	ds_read_b128 v[62:65], v103 offset:16
	ds_read_b128 v[130:133], v103 offset:32
	ds_read_b128 v[134:137], v103 offset:48
	s_waitcnt lgkmcnt(3)
	v_fmac_f32_e32 v72, v60, v34
	s_waitcnt lgkmcnt(2)
	v_fmac_f32_e32 v69, v60, v62
	v_fmac_f32_e32 v73, v60, v35
	v_fmac_f32_e32 v66, v60, v63
	v_fmac_f32_e32 v114, v60, v36
	v_fmac_f32_e32 v67, v60, v64
	v_fmac_f32_e32 v129, v60, v37
	v_fmac_f32_e32 v68, v60, v65
	ds_read_b128 v[34:37], v103 offset:64
	ds_read_b128 v[62:65], v103 offset:80
	s_waitcnt lgkmcnt(2)
	v_fmac_f32_e32 v69, v61, v134
	v_fmac_f32_e32 v66, v61, v135
	v_fmac_f32_e32 v72, v61, v130
	v_fmac_f32_e32 v73, v61, v131
	v_fmac_f32_e32 v114, v61, v132
	v_fmac_f32_e32 v67, v61, v136
	v_fmac_f32_e32 v129, v61, v133
	v_fmac_f32_e32 v68, v61, v137
	s_waitcnt lgkmcnt(0)
	v_fmac_f32_e32 v69, v58, v62
	v_fmac_f32_e32 v66, v58, v63
	ds_read_b128 v[60:63], v103 offset:96
	ds_read_b128 v[130:133], v103 offset:112
	v_fmac_f32_e32 v72, v58, v34
	v_fmac_f32_e32 v73, v58, v35
	v_fmac_f32_e32 v114, v58, v36
	v_fmac_f32_e32 v67, v58, v64
	v_fmac_f32_e32 v129, v58, v37
	v_fmac_f32_e32 v68, v58, v65
	ds_read_b128 v[34:37], v103 offset:128
	ds_read_b128 v[134:137], v103 offset:144
	s_waitcnt lgkmcnt(3)
	v_fmac_f32_e32 v72, v59, v60
	s_waitcnt lgkmcnt(2)
	v_fmac_f32_e32 v69, v59, v130
	v_fmac_f32_e32 v73, v59, v61
	v_fmac_f32_e32 v66, v59, v131
	v_fmac_f32_e32 v114, v59, v62
	v_fmac_f32_e32 v67, v59, v132
	v_fmac_f32_e32 v129, v59, v63
	v_fmac_f32_e32 v68, v59, v133
	ds_read_b128 v[58:61], v103 offset:160
	ds_read_b128 v[62:65], v103 offset:176
	s_waitcnt lgkmcnt(3)
	v_fmac_f32_e32 v72, v56, v34
	s_waitcnt lgkmcnt(2)
	v_fmac_f32_e32 v69, v56, v134
	v_fmac_f32_e32 v73, v56, v35
	v_fmac_f32_e32 v66, v56, v135
	v_fmac_f32_e32 v114, v56, v36
	v_fmac_f32_e32 v67, v56, v136
	v_fmac_f32_e32 v129, v56, v37
	v_fmac_f32_e32 v68, v56, v137
	ds_read_b128 v[34:37], v103 offset:192
	ds_read_b128 v[130:133], v103 offset:208
	s_waitcnt lgkmcnt(3)
	v_fmac_f32_e32 v72, v57, v58
	s_waitcnt lgkmcnt(2)
	v_fmac_f32_e32 v69, v57, v62
	v_fmac_f32_e32 v73, v57, v59
	v_fmac_f32_e32 v66, v57, v63
	v_fmac_f32_e32 v114, v57, v60
	v_fmac_f32_e32 v67, v57, v64
	v_fmac_f32_e32 v129, v57, v61
	v_fmac_f32_e32 v68, v57, v65
	ds_read_b128 v[56:59], v103 offset:224
	ds_read_b128 v[60:63], v103 offset:240
	s_waitcnt lgkmcnt(3)
	v_fmac_f32_e32 v72, v54, v34
	s_waitcnt lgkmcnt(2)
	v_fmac_f32_e32 v69, v54, v130
	v_fmac_f32_e32 v73, v54, v35
	v_fmac_f32_e32 v66, v54, v131
	v_fmac_f32_e32 v114, v54, v36
	v_fmac_f32_e32 v67, v54, v132
	v_fmac_f32_e32 v129, v54, v37
	v_fmac_f32_e32 v68, v54, v133
	s_waitcnt lgkmcnt(1)
	v_fmac_f32_e32 v72, v55, v56
	s_waitcnt lgkmcnt(0)
	v_fmac_f32_e32 v69, v55, v60
	v_fmac_f32_e32 v73, v55, v57
	v_fmac_f32_e32 v66, v55, v61
	v_fmac_f32_e32 v114, v55, v58
	v_fmac_f32_e32 v67, v55, v62
	v_fmac_f32_e32 v129, v55, v59
	v_fmac_f32_e32 v68, v55, v63
	ds_read_b128 v[34:37], v126
	ds_read_b128 v[54:57], v126 offset:16
	ds_read_b128 v[58:61], v126 offset:32
	ds_read_b128 v[62:65], v126 offset:48
	s_waitcnt lgkmcnt(3)
	v_fmac_f32_e32 v72, v52, v34
	s_waitcnt lgkmcnt(2)
	v_fmac_f32_e32 v69, v52, v54
	v_fmac_f32_e32 v73, v52, v35
	v_fmac_f32_e32 v66, v52, v55
	v_fmac_f32_e32 v114, v52, v36
	v_fmac_f32_e32 v67, v52, v56
	v_fmac_f32_e32 v129, v52, v37
	v_fmac_f32_e32 v68, v52, v57
	ds_read_b128 v[34:37], v126 offset:64
	ds_read_b128 v[54:57], v126 offset:80
	s_waitcnt lgkmcnt(2)
	v_fmac_f32_e32 v69, v53, v62
	v_fmac_f32_e32 v66, v53, v63
	v_fmac_f32_e32 v72, v53, v58
	v_fmac_f32_e32 v73, v53, v59
	v_fmac_f32_e32 v114, v53, v60
	v_fmac_f32_e32 v67, v53, v64
	v_fmac_f32_e32 v129, v53, v61
	v_fmac_f32_e32 v68, v53, v65
	s_waitcnt lgkmcnt(0)
	v_fmac_f32_e32 v69, v50, v54
	v_fmac_f32_e32 v66, v50, v55
	ds_read_b128 v[52:55], v126 offset:96
	ds_read_b128 v[58:61], v126 offset:112
	v_fmac_f32_e32 v72, v50, v34
	v_fmac_f32_e32 v73, v50, v35
	v_fmac_f32_e32 v114, v50, v36
	v_fmac_f32_e32 v67, v50, v56
	v_fmac_f32_e32 v129, v50, v37
	v_fmac_f32_e32 v68, v50, v57
	s_waitcnt lgkmcnt(0)
	v_fmac_f32_e32 v69, v51, v58
	v_fmac_f32_e32 v66, v51, v59
	ds_read_b128 v[34:37], v126 offset:128
	ds_read_b128 v[56:59], v126 offset:144
	v_fmac_f32_e32 v72, v51, v52
	v_fmac_f32_e32 v73, v51, v53
	v_fmac_f32_e32 v114, v51, v54
	v_fmac_f32_e32 v67, v51, v60
	v_fmac_f32_e32 v129, v51, v55
	v_fmac_f32_e32 v68, v51, v61
	s_waitcnt lgkmcnt(0)
	v_fmac_f32_e32 v69, v48, v56
	v_fmac_f32_e32 v66, v48, v57
	ds_read_b128 v[50:53], v126 offset:160
	ds_read_b128 v[54:57], v126 offset:176
	v_fmac_f32_e32 v72, v48, v34
	v_fmac_f32_e32 v73, v48, v35
	v_fmac_f32_e32 v114, v48, v36
	v_fmac_f32_e32 v67, v48, v58
	v_fmac_f32_e32 v129, v48, v37
	v_fmac_f32_e32 v68, v48, v59
	ds_read_b128 v[34:37], v126 offset:192
	ds_read_b128 v[58:61], v126 offset:208
	s_waitcnt lgkmcnt(3)
	v_fmac_f32_e32 v72, v49, v50
	s_waitcnt lgkmcnt(2)
	v_fmac_f32_e32 v69, v49, v54
	v_fmac_f32_e32 v73, v49, v51
	v_fmac_f32_e32 v66, v49, v55
	v_fmac_f32_e32 v114, v49, v52
	v_fmac_f32_e32 v67, v49, v56
	v_fmac_f32_e32 v129, v49, v53
	v_fmac_f32_e32 v68, v49, v57
	ds_read_b128 v[48:51], v126 offset:224
	ds_read_b128 v[52:55], v126 offset:240
	s_waitcnt lgkmcnt(3)
	v_fmac_f32_e32 v72, v46, v34
	s_waitcnt lgkmcnt(2)
	v_fmac_f32_e32 v69, v46, v58
	v_fmac_f32_e32 v73, v46, v35
	v_fmac_f32_e32 v66, v46, v59
	v_fmac_f32_e32 v114, v46, v36
	v_fmac_f32_e32 v67, v46, v60
	v_fmac_f32_e32 v129, v46, v37
	v_fmac_f32_e32 v68, v46, v61
	s_waitcnt lgkmcnt(1)
	v_fmac_f32_e32 v72, v47, v48
	s_waitcnt lgkmcnt(0)
	v_fmac_f32_e32 v69, v47, v52
	v_fmac_f32_e32 v73, v47, v49
	v_fmac_f32_e32 v66, v47, v53
	v_fmac_f32_e32 v114, v47, v50
	v_fmac_f32_e32 v67, v47, v54
	v_fmac_f32_e32 v129, v47, v51
	v_fmac_f32_e32 v68, v47, v55
	ds_read_b128 v[34:37], v127
	ds_read_b128 v[46:49], v127 offset:16
	ds_read_b128 v[50:53], v127 offset:32
	ds_read_b128 v[54:57], v127 offset:48
	s_waitcnt lgkmcnt(3)
	v_fmac_f32_e32 v72, v44, v34
	s_waitcnt lgkmcnt(2)
	v_fmac_f32_e32 v69, v44, v46
	v_fmac_f32_e32 v73, v44, v35
	v_fmac_f32_e32 v66, v44, v47
	v_fmac_f32_e32 v114, v44, v36
	v_fmac_f32_e32 v67, v44, v48
	v_fmac_f32_e32 v129, v44, v37
	v_fmac_f32_e32 v68, v44, v49
	ds_read_b128 v[34:37], v127 offset:64
	ds_read_b128 v[46:49], v127 offset:80
	s_waitcnt lgkmcnt(2)
	v_fmac_f32_e32 v69, v45, v54
	v_fmac_f32_e32 v66, v45, v55
	v_fmac_f32_e32 v72, v45, v50
	v_fmac_f32_e32 v73, v45, v51
	v_fmac_f32_e32 v114, v45, v52
	v_fmac_f32_e32 v67, v45, v56
	v_fmac_f32_e32 v129, v45, v53
	v_fmac_f32_e32 v68, v45, v57
	s_waitcnt lgkmcnt(0)
	v_fmac_f32_e32 v69, v42, v46
	v_fmac_f32_e32 v66, v42, v47
	ds_read_b128 v[44:47], v127 offset:96
	ds_read_b128 v[50:53], v127 offset:112
	v_fmac_f32_e32 v72, v42, v34
	v_fmac_f32_e32 v73, v42, v35
	v_fmac_f32_e32 v114, v42, v36
	v_fmac_f32_e32 v67, v42, v48
	v_fmac_f32_e32 v129, v42, v37
	v_fmac_f32_e32 v68, v42, v49
	s_waitcnt lgkmcnt(0)
	v_fmac_f32_e32 v69, v43, v50
	v_fmac_f32_e32 v66, v43, v51
	ds_read_b128 v[34:37], v127 offset:128
	ds_read_b128 v[48:51], v127 offset:144
	v_fmac_f32_e32 v72, v43, v44
	v_fmac_f32_e32 v73, v43, v45
	v_fmac_f32_e32 v114, v43, v46
	v_fmac_f32_e32 v67, v43, v52
	v_fmac_f32_e32 v129, v43, v47
	v_fmac_f32_e32 v68, v43, v53
	s_waitcnt lgkmcnt(0)
	v_fmac_f32_e32 v69, v40, v48
	v_fmac_f32_e32 v66, v40, v49
	ds_read_b128 v[42:45], v127 offset:160
	ds_read_b128 v[46:49], v127 offset:176
	v_fmac_f32_e32 v72, v40, v34
	v_fmac_f32_e32 v73, v40, v35
	v_fmac_f32_e32 v114, v40, v36
	v_fmac_f32_e32 v67, v40, v50
	v_fmac_f32_e32 v129, v40, v37
	v_fmac_f32_e32 v68, v40, v51
	ds_read_b128 v[34:37], v127 offset:192
	ds_read_b128 v[50:53], v127 offset:208
	s_waitcnt lgkmcnt(3)
	v_fmac_f32_e32 v72, v41, v42
	s_waitcnt lgkmcnt(2)
	v_fmac_f32_e32 v69, v41, v46
	v_fmac_f32_e32 v73, v41, v43
	v_fmac_f32_e32 v66, v41, v47
	v_fmac_f32_e32 v114, v41, v44
	v_fmac_f32_e32 v67, v41, v48
	v_fmac_f32_e32 v129, v41, v45
	v_fmac_f32_e32 v68, v41, v49
	ds_read_b128 v[40:43], v127 offset:224
	ds_read_b128 v[44:47], v127 offset:240
	s_waitcnt lgkmcnt(3)
	v_fmac_f32_e32 v72, v38, v34
	s_waitcnt lgkmcnt(2)
	v_fmac_f32_e32 v69, v38, v50
	v_fmac_f32_e32 v73, v38, v35
	v_fmac_f32_e32 v66, v38, v51
	v_fmac_f32_e32 v114, v38, v36
	v_fmac_f32_e32 v67, v38, v52
	v_fmac_f32_e32 v129, v38, v37
	v_fmac_f32_e32 v68, v38, v53
	s_waitcnt lgkmcnt(1)
	v_fmac_f32_e32 v72, v39, v40
	s_waitcnt lgkmcnt(0)
	v_fmac_f32_e32 v69, v39, v44
	v_fmac_f32_e32 v73, v39, v41
	v_fmac_f32_e32 v66, v39, v45
	v_fmac_f32_e32 v114, v39, v42
	v_fmac_f32_e32 v67, v39, v46
	v_fmac_f32_e32 v129, v39, v43
	v_fmac_f32_e32 v68, v39, v47
	ds_bpermute_b32 v34, v95, v72
	ds_bpermute_b32 v35, v95, v73
	ds_bpermute_b32 v36, v95, v114
	ds_bpermute_b32 v37, v95, v129
	ds_bpermute_b32 v38, v95, v69
	s_waitcnt lgkmcnt(4)
	v_add_f32_e32 v34, v72, v34
	ds_bpermute_b32 v39, v99, v34
	s_waitcnt lgkmcnt(4)
	v_add_f32_e32 v35, v73, v35
	ds_bpermute_b32 v40, v99, v35
	s_waitcnt lgkmcnt(4)
	v_add_f32_e32 v36, v114, v36
	ds_bpermute_b32 v41, v99, v36
	s_waitcnt lgkmcnt(2)
	v_add_f32_e32 v34, v34, v39
	ds_bpermute_b32 v39, v122, v34
	s_waitcnt lgkmcnt(2)
	v_add_f32_e32 v35, v35, v40
	ds_bpermute_b32 v40, v122, v35
	v_add_f32_e32 v37, v129, v37
	v_add_f32_e32 v38, v69, v38
	s_waitcnt lgkmcnt(1)
	v_add_f32_e32 v34, v34, v39
	ds_bpermute_b32 v39, v123, v34
	v_add_f32_e32 v36, v36, v41
	s_waitcnt lgkmcnt(1)
	v_add_f32_e32 v35, v35, v40
	ds_bpermute_b32 v41, v122, v36
	ds_bpermute_b32 v40, v123, v35
	s_waitcnt lgkmcnt(2)
	v_add_f32_e32 v34, v34, v39
	ds_bpermute_b32 v39, v124, v34
	ds_bpermute_b32 v42, v99, v37
	s_waitcnt lgkmcnt(3)
	v_add_f32_e32 v41, v36, v41
	s_waitcnt lgkmcnt(2)
	v_add_f32_e32 v36, v35, v40
	ds_bpermute_b32 v40, v124, v36
	s_waitcnt lgkmcnt(2)
	v_add_f32_e32 v34, v34, v39
	ds_bpermute_b32 v39, v99, v38
	s_waitcnt lgkmcnt(2)
	v_add_f32_e32 v37, v37, v42
	ds_bpermute_b32 v43, v123, v41
	ds_bpermute_b32 v42, v122, v37
	s_waitcnt lgkmcnt(3)
	v_add_f32_e32 v36, v36, v40
	s_waitcnt lgkmcnt(2)
	v_add_f32_e32 v38, v38, v39
	ds_bpermute_b32 v39, v122, v38
	s_waitcnt lgkmcnt(2)
	v_add_f32_e32 v40, v41, v43
	s_waitcnt lgkmcnt(1)
	v_add_f32_e32 v41, v37, v42
	ds_bpermute_b32 v42, v123, v41
	ds_bpermute_b32 v43, v124, v40
	s_waitcnt lgkmcnt(2)
	v_add_f32_e32 v39, v38, v39
	ds_bpermute_b32 v44, v123, v39
	ds_bpermute_b32 v45, v95, v66
	s_waitcnt lgkmcnt(3)
	v_add_f32_e32 v41, v41, v42
	s_waitcnt lgkmcnt(2)
	v_add_f32_e32 v38, v40, v43
	ds_bpermute_b32 v42, v124, v41
	s_waitcnt lgkmcnt(2)
	v_add_f32_e32 v43, v39, v44
	ds_bpermute_b32 v44, v124, v43
	ds_bpermute_b32 v46, v95, v68
	s_waitcnt lgkmcnt(3)
	v_add_f32_e32 v45, v66, v45
	s_waitcnt lgkmcnt(2)
	v_add_f32_e32 v40, v41, v42
	ds_bpermute_b32 v47, v99, v45
	s_waitcnt lgkmcnt(2)
	v_add_f32_e32 v42, v43, v44
	ds_bpermute_b32 v44, v95, v67
	s_waitcnt lgkmcnt(2)
	v_add_f32_e32 v46, v68, v46
	ds_bpermute_b32 v49, v99, v46
	s_waitcnt lgkmcnt(2)
	v_add_f32_e32 v45, v45, v47
	ds_bpermute_b32 v47, v122, v45
	s_waitcnt lgkmcnt(2)
	v_add_f32_e32 v44, v67, v44
	ds_bpermute_b32 v48, v99, v44
	s_waitcnt lgkmcnt(2)
	v_add_f32_e32 v46, v46, v49
	ds_bpermute_b32 v49, v122, v46
	s_waitcnt lgkmcnt(2)
	v_add_f32_e32 v45, v45, v47
	ds_bpermute_b32 v47, v123, v45
	s_waitcnt lgkmcnt(2)
	v_add_f32_e32 v44, v44, v48
	ds_bpermute_b32 v48, v122, v44
	s_waitcnt lgkmcnt(2)
	v_add_f32_e32 v46, v46, v49
	ds_bpermute_b32 v49, v123, v46
	s_waitcnt lgkmcnt(2)
	v_add_f32_e32 v45, v45, v47
	ds_bpermute_b32 v47, v124, v45
	s_waitcnt lgkmcnt(2)
	v_add_f32_e32 v44, v44, v48
	ds_bpermute_b32 v48, v123, v44
	s_waitcnt lgkmcnt(2)
	v_add_f32_e32 v49, v46, v49
	ds_bpermute_b32 v51, v124, v49
	ds_bpermute_b32 v35, v125, v34
	ds_bpermute_b32 v37, v125, v36
	s_waitcnt lgkmcnt(3)
	v_add_f32_e32 v48, v44, v48
	ds_bpermute_b32 v50, v124, v48
	v_add_f32_e32 v44, v45, v47
	ds_bpermute_b32 v39, v125, v38
	ds_bpermute_b32 v41, v125, v40
	ds_bpermute_b32 v43, v125, v42
	s_waitcnt lgkmcnt(3)
	v_add_f32_e32 v46, v48, v50
	v_add_f32_e32 v48, v49, v51
	ds_bpermute_b32 v45, v125, v44
	ds_bpermute_b32 v47, v125, v46
	ds_bpermute_b32 v49, v125, v48
	s_and_saveexec_b64 s[20:21], s[18:19]
	s_cbranch_execz .LBB0_37
	s_load_dwordx2 s[76:77], s[30:31], 0x20
	v_add_f32_e32 v36, v36, v37
	v_add_f32_e32 v34, v34, v35
	s_waitcnt lgkmcnt(0)
	v_add_f32_e32 v38, v38, v39
	v_cndmask_b32_e64 v34, v34, v36, s[4:5]
	global_load_dword v50, v128, s[76:77]
	v_add_f32_e32 v40, v40, v41
	v_cndmask_b32_e64 v34, v34, v38, s[6:7]
	v_add_f32_e32 v42, v42, v43
	v_cndmask_b32_e64 v34, v34, v40, s[8:9]
	v_add_f32_e32 v44, v44, v45
	v_cndmask_b32_e64 v34, v34, v42, s[10:11]
	v_add_f32_e32 v46, v46, v47
	v_cndmask_b32_e64 v34, v34, v44, s[12:13]
	v_add_f32_e32 v48, v48, v49
	v_cndmask_b32_e64 v34, v34, v46, s[14:15]
	v_cndmask_b32_e64 v34, v34, v48, s[16:17]
	s_waitcnt vmcnt(0)
	v_add_f32_e32 v36, v34, v50
	v_lshl_add_u64 v[34:35], s[34:35], 0, v[110:111]
	global_store_dword v[34:35], v36, off
	s_branch .LBB0_37

.LBB0_728:
	v_lshl_add_u64 v[184:185], s[92:93], 0, v[154:155]
	v_lshl_add_u64 v[188:189], s[92:93], 0, v[156:157]
	v_lshl_add_u64 v[192:193], s[92:93], 0, v[158:159]
	v_lshl_add_u64 v[196:197], s[92:93], 0, v[160:161]
	v_lshl_add_u64 v[200:201], s[92:93], 0, v[162:163]
	v_lshl_add_u64 v[204:205], s[92:93], 0, v[164:165]
	v_lshl_add_u64 v[210:211], s[92:93], 0, v[166:167]
	v_lshl_add_u64 v[214:215], s[92:93], 0, v[168:169]
	global_load_dwordx4 v[184:187], v[184:185], off
	s_nop 0
	global_load_dwordx4 v[188:191], v[188:189], off
	s_nop 0
	global_load_dwordx4 v[192:195], v[192:193], off
	s_nop 0
	global_load_dwordx4 v[196:199], v[196:197], off
	s_nop 0
	global_load_dwordx4 v[200:203], v[200:201], off
	s_nop 0
	global_load_dwordx4 v[204:207], v[204:205], off
	s_nop 0
	global_load_dwordx4 v[210:213], v[210:211], off
	s_nop 0
	global_load_dwordx4 v[214:217], v[214:215], off
	v_add_u32_e32 v218, v182, v153
	v_add_u32_e32 v219, v182, v171
	v_add_u32_e32 v220, v182, v172
	v_add_u32_e32 v221, v182, v173
	v_add_u32_e32 v222, v182, v174
	v_add_u32_e32 v223, v182, v175
	v_add_u32_e32 v224, v182, v176
	v_add_u32_e32 v225, v182, v177
	v_lshl_add_u64 v[154:155], v[154:155], 0, s[8:9]
	v_lshl_add_u64 v[156:157], v[156:157], 0, s[8:9]
	v_lshl_add_u64 v[158:159], v[158:159], 0, s[8:9]
	v_lshl_add_u64 v[160:161], v[160:161], 0, s[8:9]
	v_lshl_add_u64 v[162:163], v[162:163], 0, s[8:9]
	v_lshl_add_u64 v[164:165], v[164:165], 0, s[8:9]
	v_lshl_add_u64 v[166:167], v[166:167], 0, s[8:9]
	v_lshl_add_u64 v[168:169], v[168:169], 0, s[8:9]
	s_waitcnt vmcnt(7)
	ds_write_b128 v218, v[184:187]
	s_waitcnt vmcnt(6)
	ds_write_b128 v219, v[188:191]
	s_waitcnt vmcnt(5)
	ds_write_b128 v220, v[192:195]
	s_waitcnt vmcnt(4)
	ds_write_b128 v221, v[196:199]
	s_waitcnt vmcnt(3)
	ds_write_b128 v222, v[200:203]
	s_waitcnt vmcnt(2)
	ds_write_b128 v223, v[204:207]
	s_waitcnt vmcnt(1)
	ds_write_b128 v224, v[210:213]
	s_waitcnt vmcnt(0)
	ds_write_b128 v225, v[214:217]
	s_waitcnt lgkmcnt(0)
	s_barrier
	ds_read_b128 v[184:187], v183
	ds_read_b128 v[188:191], v183 offset:64
	ds_read_b128 v[192:195], v183 offset:33024
	ds_read_b128 v[196:199], v183 offset:33088
	s_waitcnt lgkmcnt(3)
	v_mfma_f32_16x16x32_f16 v[184:187], v[4:7], v[184:187], 0
	v_add_u32_e32 v204, s1, v2
	s_addk_i32 s1, 0x4080
	s_cmp_eq_u32 s0, s1
	s_waitcnt lgkmcnt(1)
	v_mfma_f32_16x16x32_f16 v[192:195], v[4:7], v[192:195], 0
	v_mfma_f32_16x16x32_f16 v[184:187], v[8:11], v[188:191], v[184:187]
	s_waitcnt lgkmcnt(0)
	v_mfma_f32_16x16x32_f16 v[188:191], v[8:11], v[196:199], v[192:195]
	s_nop 4
	ds_read_b128 v[192:195], v183 offset:128
	ds_read_b128 v[196:199], v183 offset:192
	s_waitcnt lgkmcnt(1)
	v_mfma_f32_16x16x32_f16 v[184:187], v[12:15], v[192:195], v[184:187]
	ds_read_b128 v[192:195], v183 offset:33152
	ds_read_b128 v[200:203], v183 offset:33216
	s_waitcnt lgkmcnt(1)
	v_mfma_f32_16x16x32_f16 v[188:191], v[12:15], v[192:195], v[188:191]
	v_mfma_f32_16x16x32_f16 v[184:187], v[16:19], v[196:199], v[184:187]
	ds_read_b128 v[192:195], v183 offset:256
	ds_read_b128 v[196:199], v183 offset:320
	s_waitcnt lgkmcnt(2)
	v_mfma_f32_16x16x32_f16 v[188:191], v[16:19], v[200:203], v[188:191]
	s_waitcnt lgkmcnt(1)
	v_mfma_f32_16x16x32_f16 v[184:187], v[20:23], v[192:195], v[184:187]
	ds_read_b128 v[192:195], v183 offset:33280
	ds_read_b128 v[200:203], v183 offset:33344
	s_waitcnt lgkmcnt(1)
	v_mfma_f32_16x16x32_f16 v[188:191], v[20:23], v[192:195], v[188:191]
	v_mfma_f32_16x16x32_f16 v[184:187], v[24:27], v[196:199], v[184:187]
	ds_read_b128 v[192:195], v183 offset:384
	ds_read_b128 v[196:199], v183 offset:448
	s_waitcnt lgkmcnt(2)
	v_mfma_f32_16x16x32_f16 v[188:191], v[24:27], v[200:203], v[188:191]
	s_waitcnt lgkmcnt(1)
	v_mfma_f32_16x16x32_f16 v[184:187], v[28:31], v[192:195], v[184:187]
	ds_read_b128 v[192:195], v183 offset:33408
	ds_read_b128 v[200:203], v183 offset:33472
	s_waitcnt lgkmcnt(1)
	v_mfma_f32_16x16x32_f16 v[188:191], v[28:31], v[192:195], v[188:191]
	v_mfma_f32_16x16x32_f16 v[184:187], v[32:35], v[196:199], v[184:187]
	ds_read_b128 v[192:195], v183 offset:512
	ds_read_b128 v[196:199], v183 offset:576
	s_waitcnt lgkmcnt(2)
	v_mfma_f32_16x16x32_f16 v[188:191], v[32:35], v[200:203], v[188:191]
	s_waitcnt lgkmcnt(1)
	v_mfma_f32_16x16x32_f16 v[184:187], v[36:39], v[192:195], v[184:187]
	ds_read_b128 v[192:195], v183 offset:33536
	ds_read_b128 v[200:203], v183 offset:33600
	s_waitcnt lgkmcnt(1)
	v_mfma_f32_16x16x32_f16 v[188:191], v[36:39], v[192:195], v[188:191]
	v_mfma_f32_16x16x32_f16 v[184:187], v[40:43], v[196:199], v[184:187]
	ds_read_b128 v[192:195], v183 offset:640
	ds_read_b128 v[196:199], v183 offset:704
	s_waitcnt lgkmcnt(2)
	v_mfma_f32_16x16x32_f16 v[188:191], v[40:43], v[200:203], v[188:191]
	s_waitcnt lgkmcnt(1)
	v_mfma_f32_16x16x32_f16 v[184:187], v[44:47], v[192:195], v[184:187]
	ds_read_b128 v[192:195], v183 offset:33664
	ds_read_b128 v[200:203], v183 offset:33728
	s_waitcnt lgkmcnt(1)
	v_mfma_f32_16x16x32_f16 v[188:191], v[44:47], v[192:195], v[188:191]
	v_mfma_f32_16x16x32_f16 v[184:187], v[48:51], v[196:199], v[184:187]
	ds_read_b128 v[192:195], v183 offset:768
	ds_read_b128 v[196:199], v183 offset:832
	s_waitcnt lgkmcnt(2)
	v_mfma_f32_16x16x32_f16 v[188:191], v[48:51], v[200:203], v[188:191]
	s_waitcnt lgkmcnt(1)
	v_mfma_f32_16x16x32_f16 v[184:187], v[52:55], v[192:195], v[184:187]
	ds_read_b128 v[192:195], v183 offset:33792
	ds_read_b128 v[200:203], v183 offset:33856
	s_waitcnt lgkmcnt(1)
	v_mfma_f32_16x16x32_f16 v[188:191], v[52:55], v[192:195], v[188:191]
	v_mfma_f32_16x16x32_f16 v[184:187], v[56:59], v[196:199], v[184:187]
	ds_read_b128 v[192:195], v183 offset:896
	ds_read_b128 v[196:199], v183 offset:960
	s_waitcnt lgkmcnt(2)
	v_mfma_f32_16x16x32_f16 v[188:191], v[56:59], v[200:203], v[188:191]
	s_waitcnt lgkmcnt(1)
	v_mfma_f32_16x16x32_f16 v[184:187], v[60:63], v[192:195], v[184:187]
	ds_read_b128 v[192:195], v183 offset:33920
	ds_read_b128 v[200:203], v183 offset:33984
	s_waitcnt lgkmcnt(1)
	v_mfma_f32_16x16x32_f16 v[188:191], v[60:63], v[192:195], v[188:191]
	v_mfma_f32_16x16x32_f16 v[184:187], v[64:67], v[196:199], v[184:187]
	ds_read_b128 v[192:195], v183 offset:1024
	ds_read_b128 v[196:199], v183 offset:1088
	s_waitcnt lgkmcnt(2)
	v_mfma_f32_16x16x32_f16 v[188:191], v[64:67], v[200:203], v[188:191]
	s_waitcnt lgkmcnt(1)
	v_mfma_f32_16x16x32_f16 v[184:187], v[68:71], v[192:195], v[184:187]
	ds_read_b128 v[192:195], v183 offset:34048
	ds_read_b128 v[200:203], v183 offset:34112
	s_waitcnt lgkmcnt(1)
	v_mfma_f32_16x16x32_f16 v[188:191], v[68:71], v[192:195], v[188:191]
	v_mfma_f32_16x16x32_f16 v[184:187], v[72:75], v[196:199], v[184:187]
	ds_read_b128 v[192:195], v183 offset:1152
	ds_read_b128 v[196:199], v183 offset:1216
	s_waitcnt lgkmcnt(2)
	v_mfma_f32_16x16x32_f16 v[188:191], v[72:75], v[200:203], v[188:191]
	s_waitcnt lgkmcnt(1)
	v_mfma_f32_16x16x32_f16 v[184:187], v[76:79], v[192:195], v[184:187]
	ds_read_b128 v[192:195], v183 offset:34176
	ds_read_b128 v[200:203], v183 offset:34240
	s_waitcnt lgkmcnt(1)
	v_mfma_f32_16x16x32_f16 v[188:191], v[76:79], v[192:195], v[188:191]
	v_mfma_f32_16x16x32_f16 v[184:187], v[80:83], v[196:199], v[184:187]
	ds_read_b128 v[192:195], v183 offset:1280
	ds_read_b128 v[196:199], v183 offset:1344
	s_waitcnt lgkmcnt(2)
	v_mfma_f32_16x16x32_f16 v[188:191], v[80:83], v[200:203], v[188:191]
	s_waitcnt lgkmcnt(1)
	v_mfma_f32_16x16x32_f16 v[184:187], v[84:87], v[192:195], v[184:187]
	ds_read_b128 v[192:195], v183 offset:34304
	ds_read_b128 v[200:203], v183 offset:34368
	s_waitcnt lgkmcnt(1)
	v_mfma_f32_16x16x32_f16 v[188:191], v[84:87], v[192:195], v[188:191]
	v_mfma_f32_16x16x32_f16 v[184:187], v[88:91], v[196:199], v[184:187]
	ds_read_b128 v[192:195], v183 offset:1408
	ds_read_b128 v[196:199], v183 offset:1472
	s_waitcnt lgkmcnt(2)
	v_mfma_f32_16x16x32_f16 v[188:191], v[88:91], v[200:203], v[188:191]
	s_waitcnt lgkmcnt(1)
	v_mfma_f32_16x16x32_f16 v[184:187], v[92:95], v[192:195], v[184:187]
	ds_read_b128 v[192:195], v183 offset:34432
	ds_read_b128 v[200:203], v183 offset:34496
	s_waitcnt lgkmcnt(1)
	v_mfma_f32_16x16x32_f16 v[188:191], v[92:95], v[192:195], v[188:191]
	v_mfma_f32_16x16x32_f16 v[184:187], v[96:99], v[196:199], v[184:187]
	ds_read_b128 v[192:195], v183 offset:1536
	ds_read_b128 v[196:199], v183 offset:1600
	s_waitcnt lgkmcnt(2)
	v_mfma_f32_16x16x32_f16 v[188:191], v[96:99], v[200:203], v[188:191]
	s_waitcnt lgkmcnt(1)
	v_mfma_f32_16x16x32_f16 v[184:187], v[100:103], v[192:195], v[184:187]
	ds_read_b128 v[192:195], v183 offset:34560
	ds_read_b128 v[200:203], v183 offset:34624
	s_waitcnt lgkmcnt(1)
	v_mfma_f32_16x16x32_f16 v[188:191], v[100:103], v[192:195], v[188:191]
	v_mfma_f32_16x16x32_f16 v[184:187], v[104:107], v[196:199], v[184:187]
	ds_read_b128 v[192:195], v183 offset:1664
	ds_read_b128 v[196:199], v183 offset:1728
	s_waitcnt lgkmcnt(2)
	v_mfma_f32_16x16x32_f16 v[188:191], v[104:107], v[200:203], v[188:191]
	s_waitcnt lgkmcnt(1)
	v_mfma_f32_16x16x32_f16 v[184:187], v[108:111], v[192:195], v[184:187]
	ds_read_b128 v[192:195], v183 offset:34688
	ds_read_b128 v[200:203], v183 offset:34752
	s_waitcnt lgkmcnt(1)
	v_mfma_f32_16x16x32_f16 v[188:191], v[108:111], v[192:195], v[188:191]
	v_mfma_f32_16x16x32_f16 v[184:187], v[112:115], v[196:199], v[184:187]
	ds_read_b128 v[192:195], v183 offset:1792
	ds_read_b128 v[196:199], v183 offset:1856
	s_waitcnt lgkmcnt(2)
	v_mfma_f32_16x16x32_f16 v[188:191], v[112:115], v[200:203], v[188:191]
	s_waitcnt lgkmcnt(1)
	v_mfma_f32_16x16x32_f16 v[184:187], v[116:119], v[192:195], v[184:187]
	ds_read_b128 v[192:195], v183 offset:34816
	ds_read_b128 v[200:203], v183 offset:34880
	s_waitcnt lgkmcnt(1)
	v_mfma_f32_16x16x32_f16 v[188:191], v[116:119], v[192:195], v[188:191]
	v_mfma_f32_16x16x32_f16 v[184:187], v[120:123], v[196:199], v[184:187]
	ds_read_b128 v[192:195], v183 offset:1920
	ds_read_b128 v[196:199], v183 offset:1984
	s_waitcnt lgkmcnt(2)
	v_mfma_f32_16x16x32_f16 v[188:191], v[120:123], v[200:203], v[188:191]
	s_waitcnt lgkmcnt(1)
	v_mfma_f32_16x16x32_f16 v[184:187], v[124:127], v[192:195], v[184:187]
	ds_read_b128 v[192:195], v183 offset:34944
	ds_read_b128 v[200:203], v183 offset:35008
	s_waitcnt lgkmcnt(1)
	v_mfma_f32_16x16x32_f16 v[188:191], v[124:127], v[192:195], v[188:191]
	v_add_u32_e32 v192, 0x10a00, v204
	v_add_u32_e32 v193, 0x10a08, v204
	v_add_u32_e32 v194, 0x12a40, v204
	v_mfma_f32_16x16x32_f16 v[184:187], v[128:131], v[196:199], v[184:187]
	v_add_u32_e32 v195, 0x12a48, v204
	s_waitcnt lgkmcnt(0)
	v_mfma_f32_16x16x32_f16 v[188:191], v[128:131], v[200:203], v[188:191]
	s_nop 4
	ds_write2_b32 v192, v184, v185 offset1:1
	ds_write2_b32 v193, v186, v187 offset1:1
	s_nop 0
	ds_write2_b32 v194, v188, v189 offset1:1
	ds_write2_b32 v195, v190, v191 offset1:1
	s_waitcnt lgkmcnt(0)
	s_barrier
	s_cbranch_scc0 .LBB0_728
	v_cmp_lt_i32_e32 vcc, 63, v152
	s_and_saveexec_b64 s[0:1], vcc
	s_xor_b64 s[0:1], exec, s[0:1]
	s_cbranch_execz .LBB0_734
	s_movk_i32 s18, 0x860
	v_cmp_gt_u32_e32 vcc, s18, v152
	s_and_saveexec_b64 s[18:19], vcc
	s_cbranch_execz .LBB0_733
	s_mul_i32 s20, s23, 0x8200
	s_add_u32 s20, s41, s20
	v_add_u32_e32 v2, 0xfffffc00, v181
	s_addc_u32 s21, s42, 0
	v_add_u32_e32 v6, 0xfffffe00, v152
	v_add_u32_e32 v7, s44, v181
	v_lshl_add_u64 v[4:5], s[20:21], 0, v[2:3]
	s_mov_b64 s[26:27], 0x1c00
	v_lshl_add_u64 v[246:247], v[4:5], 0, s[26:27]
	v_lshl_add_u64 v[248:249], v[246:247], 0, s[26:27]
	v_lshl_add_u64 v[250:251], v[248:249], 0, s[26:27]
	v_lshl_add_u64 v[252:253], v[250:251], 0, s[26:27]
	global_load_dwordx4 v[226:229], v[4:5], off
	global_load_dwordx4 v[230:233], v[246:247], off
	global_load_dwordx4 v[234:237], v[248:249], off
	global_load_dwordx4 v[238:241], v[250:251], off
	s_movk_i32 s25, 0x160
	v_cmp_gt_u32_e32 vcc, s25, v152
	s_and_saveexec_b64 s[20:21], vcc
	s_cbranch_execz .Lssm_kt_l5
	global_load_dwordx4 v[242:245], v[252:253], off
.Lssm_kt_l5:
	s_or_b64 exec, exec, s[20:21]
	s_waitcnt vmcnt(0)
	ds_write_b128 v7, v[226:229]
	ds_write_b128 v7, v[230:233] offset:7168
	ds_write_b128 v7, v[234:237] offset:14336
	ds_write_b128 v7, v[238:241] offset:21504
	s_and_saveexec_b64 s[20:21], vcc
	s_cbranch_execz .Lssm_kt_w5
	ds_write_b128 v7, v[242:245] offset:28672
.Lssm_kt_w5:
	s_or_b64 exec, exec, s[20:21]
.LBB0_733:
	s_or_b64 exec, exec, s[18:19]

.LBB0_738:
	v_lshl_or_b32 v2, s6, 5, v170
	v_mad_u64_u32 v[88:89], s[62:63], v2, s46, v[86:87]
	ds_read_b128 v[96:99], v88
	ds_read_b128 v[100:103], v88 offset:4352
	global_load_dwordx4 v[104:107], v[70:71], off
	global_load_dwordx4 v[226:229], v[72:73], off
	global_load_dwordx4 v[230:233], v[74:75], off
	global_load_dwordx4 v[234:237], v[76:77], off
	global_load_dwordx4 v[238:241], v[78:79], off
	global_load_dwordx4 v[242:245], v[80:81], off
	global_load_dwordx4 v[246:249], v[82:83], off
	global_load_dwordx4 v[250:253], v[84:85], off
	v_lshl_or_b32 v2, s6, 11, v92
	s_add_i32 s6, s6, 1
	s_cmp_eq_u32 s6, s47
	s_waitcnt vmcnt(7) lgkmcnt(1)
	v_mfma_f32_16x16x32_f16 v[64:67], v[104:107], v[96:99], v[64:67]
	s_waitcnt lgkmcnt(0)
	v_mfma_f32_16x16x32_f16 v[60:63], v[104:107], v[100:103], v[60:63]
	global_load_dwordx4 v[104:107], v[70:71], off offset:64
	s_waitcnt vmcnt(7)
	v_mfma_f32_16x16x32_f16 v[56:59], v[226:229], v[96:99], v[56:59]
	v_mfma_f32_16x16x32_f16 v[52:55], v[226:229], v[100:103], v[52:55]
	global_load_dwordx4 v[226:229], v[72:73], off offset:64
	s_waitcnt vmcnt(7)
	v_mfma_f32_16x16x32_f16 v[48:51], v[230:233], v[96:99], v[48:51]
	v_mfma_f32_16x16x32_f16 v[44:47], v[230:233], v[100:103], v[44:47]
	global_load_dwordx4 v[230:233], v[74:75], off offset:64
	s_waitcnt vmcnt(7)
	v_mfma_f32_16x16x32_f16 v[40:43], v[234:237], v[96:99], v[40:43]
	v_mfma_f32_16x16x32_f16 v[36:39], v[234:237], v[100:103], v[36:39]
	global_load_dwordx4 v[234:237], v[76:77], off offset:64
	s_waitcnt vmcnt(7)
	v_mfma_f32_16x16x32_f16 v[32:35], v[238:241], v[96:99], v[32:35]
	v_mfma_f32_16x16x32_f16 v[28:31], v[238:241], v[100:103], v[28:31]
	global_load_dwordx4 v[238:241], v[78:79], off offset:64
	s_waitcnt vmcnt(7)
	v_mfma_f32_16x16x32_f16 v[24:27], v[242:245], v[96:99], v[24:27]
	v_mfma_f32_16x16x32_f16 v[20:23], v[242:245], v[100:103], v[20:23]
	global_load_dwordx4 v[242:245], v[80:81], off offset:64
	s_waitcnt vmcnt(7)
	v_mfma_f32_16x16x32_f16 v[16:19], v[246:249], v[96:99], v[16:19]
	v_mfma_f32_16x16x32_f16 v[12:15], v[246:249], v[100:103], v[12:15]
	global_load_dwordx4 v[246:249], v[82:83], off offset:64
	s_waitcnt vmcnt(7)
	v_mfma_f32_16x16x32_f16 v[8:11], v[250:253], v[96:99], v[8:11]
	v_mfma_f32_16x16x32_f16 v[4:7], v[250:253], v[100:103], v[4:7]
	global_load_dwordx4 v[250:253], v[84:85], off offset:64
	ds_read_b128 v[96:99], v88 offset:64
	ds_read_b128 v[100:103], v88 offset:4416
	s_waitcnt vmcnt(7) lgkmcnt(1)
	v_mfma_f32_16x16x32_f16 v[64:67], v[104:107], v[96:99], v[64:67]
	s_waitcnt lgkmcnt(0)
	v_mfma_f32_16x16x32_f16 v[60:63], v[104:107], v[100:103], v[60:63]
	global_load_dwordx4 v[104:107], v[70:71], off offset:128
	s_waitcnt vmcnt(7)
	v_mfma_f32_16x16x32_f16 v[56:59], v[226:229], v[96:99], v[56:59]
	v_mfma_f32_16x16x32_f16 v[52:55], v[226:229], v[100:103], v[52:55]
	global_load_dwordx4 v[226:229], v[72:73], off offset:128
	s_waitcnt vmcnt(7)
	v_mfma_f32_16x16x32_f16 v[48:51], v[230:233], v[96:99], v[48:51]
	v_mfma_f32_16x16x32_f16 v[44:47], v[230:233], v[100:103], v[44:47]
	global_load_dwordx4 v[230:233], v[74:75], off offset:128
	s_waitcnt vmcnt(7)
	v_mfma_f32_16x16x32_f16 v[40:43], v[234:237], v[96:99], v[40:43]
	v_mfma_f32_16x16x32_f16 v[36:39], v[234:237], v[100:103], v[36:39]
	global_load_dwordx4 v[234:237], v[76:77], off offset:128
	s_waitcnt vmcnt(7)
	v_mfma_f32_16x16x32_f16 v[32:35], v[238:241], v[96:99], v[32:35]
	v_mfma_f32_16x16x32_f16 v[28:31], v[238:241], v[100:103], v[28:31]
	global_load_dwordx4 v[238:241], v[78:79], off offset:128
	s_waitcnt vmcnt(7)
	v_mfma_f32_16x16x32_f16 v[24:27], v[242:245], v[96:99], v[24:27]
	v_mfma_f32_16x16x32_f16 v[20:23], v[242:245], v[100:103], v[20:23]
	global_load_dwordx4 v[242:245], v[80:81], off offset:128
	s_waitcnt vmcnt(7)
	v_mfma_f32_16x16x32_f16 v[16:19], v[246:249], v[96:99], v[16:19]
	v_mfma_f32_16x16x32_f16 v[12:15], v[246:249], v[100:103], v[12:15]
	global_load_dwordx4 v[246:249], v[82:83], off offset:128
	s_waitcnt vmcnt(7)
	v_mfma_f32_16x16x32_f16 v[8:11], v[250:253], v[96:99], v[8:11]
	v_mfma_f32_16x16x32_f16 v[4:7], v[250:253], v[100:103], v[4:7]
	global_load_dwordx4 v[250:253], v[84:85], off offset:128
	ds_read_b128 v[96:99], v88 offset:128
	ds_read_b128 v[100:103], v88 offset:4480
	s_waitcnt vmcnt(7) lgkmcnt(1)
	v_mfma_f32_16x16x32_f16 v[64:67], v[104:107], v[96:99], v[64:67]
	s_waitcnt lgkmcnt(0)
	v_mfma_f32_16x16x32_f16 v[60:63], v[104:107], v[100:103], v[60:63]
	global_load_dwordx4 v[104:107], v[70:71], off offset:192
	s_waitcnt vmcnt(7)
	v_mfma_f32_16x16x32_f16 v[56:59], v[226:229], v[96:99], v[56:59]
	v_mfma_f32_16x16x32_f16 v[52:55], v[226:229], v[100:103], v[52:55]
	global_load_dwordx4 v[226:229], v[72:73], off offset:192
	s_waitcnt vmcnt(7)
	v_mfma_f32_16x16x32_f16 v[48:51], v[230:233], v[96:99], v[48:51]
	v_mfma_f32_16x16x32_f16 v[44:47], v[230:233], v[100:103], v[44:47]
	global_load_dwordx4 v[230:233], v[74:75], off offset:192
	s_waitcnt vmcnt(7)
	v_mfma_f32_16x16x32_f16 v[40:43], v[234:237], v[96:99], v[40:43]
	v_mfma_f32_16x16x32_f16 v[36:39], v[234:237], v[100:103], v[36:39]
	global_load_dwordx4 v[234:237], v[76:77], off offset:192
	s_waitcnt vmcnt(7)
	v_mfma_f32_16x16x32_f16 v[32:35], v[238:241], v[96:99], v[32:35]
	v_mfma_f32_16x16x32_f16 v[28:31], v[238:241], v[100:103], v[28:31]
	global_load_dwordx4 v[238:241], v[78:79], off offset:192
	s_waitcnt vmcnt(7)
	v_mfma_f32_16x16x32_f16 v[24:27], v[242:245], v[96:99], v[24:27]
	v_mfma_f32_16x16x32_f16 v[20:23], v[242:245], v[100:103], v[20:23]
	global_load_dwordx4 v[242:245], v[80:81], off offset:192
	s_waitcnt vmcnt(7)
	v_mfma_f32_16x16x32_f16 v[16:19], v[246:249], v[96:99], v[16:19]
	v_mfma_f32_16x16x32_f16 v[12:15], v[246:249], v[100:103], v[12:15]
	global_load_dwordx4 v[246:249], v[82:83], off offset:192
	s_waitcnt vmcnt(7)
	v_mfma_f32_16x16x32_f16 v[8:11], v[250:253], v[96:99], v[8:11]
	v_mfma_f32_16x16x32_f16 v[4:7], v[250:253], v[100:103], v[4:7]
	global_load_dwordx4 v[250:253], v[84:85], off offset:192
	ds_read_b128 v[96:99], v88 offset:192
	ds_read_b128 v[100:103], v88 offset:4544
	v_lshl_add_u64 v[88:89], s[18:19], 0, v[2:3]
	s_waitcnt vmcnt(7) lgkmcnt(1)
	v_mfma_f32_16x16x32_f16 v[64:67], v[104:107], v[96:99], v[64:67]
	s_nop 7
	v_mul_f32_e32 v95, 0x3d372713, v64
	s_waitcnt lgkmcnt(0)
	v_mfma_f32_16x16x32_f16 v[60:63], v[104:107], v[100:103], v[60:63]
	v_mul_f32_e32 v95, v64, v95
	v_fma_f32 v95, v64, v95, v64
	s_waitcnt vmcnt(6)
	v_mfma_f32_16x16x32_f16 v[56:59], v[226:229], v[96:99], v[56:59]
	v_mul_f32_e32 v95, 0x3f4c422a, v95
	v_add_f32_e32 v95, v95, v95
	v_mul_f32_e32 v95, 0x3fb8aa3b, v95
	v_mfma_f32_16x16x32_f16 v[52:55], v[226:229], v[100:103], v[52:55]
	v_exp_f32_e32 v95, v95
	s_waitcnt vmcnt(5)
	v_mfma_f32_16x16x32_f16 v[48:51], v[230:233], v[96:99], v[48:51]
	v_add_f32_e32 v95, 1.0, v95
	v_mfma_f32_16x16x32_f16 v[44:47], v[230:233], v[100:103], v[44:47]
	s_waitcnt vmcnt(4)
	v_mfma_f32_16x16x32_f16 v[40:43], v[234:237], v[96:99], v[40:43]
	v_mfma_f32_16x16x32_f16 v[36:39], v[234:237], v[100:103], v[36:39]
	s_waitcnt vmcnt(3)
	v_mfma_f32_16x16x32_f16 v[32:35], v[238:241], v[96:99], v[32:35]
	v_mfma_f32_16x16x32_f16 v[28:31], v[238:241], v[100:103], v[28:31]
	s_waitcnt vmcnt(2)
	v_mfma_f32_16x16x32_f16 v[24:27], v[242:245], v[96:99], v[24:27]
	v_mfma_f32_16x16x32_f16 v[20:23], v[242:245], v[100:103], v[20:23]
	s_waitcnt vmcnt(1)
	v_mfma_f32_16x16x32_f16 v[16:19], v[246:249], v[96:99], v[16:19]
	v_mfma_f32_16x16x32_f16 v[12:15], v[246:249], v[100:103], v[12:15]
	s_waitcnt vmcnt(0)
	v_mfma_f32_16x16x32_f16 v[8:11], v[250:253], v[96:99], v[8:11]
	v_rcp_f32_e32 v96, v95
	v_mul_f32_e32 v95, 0x3d372713, v65
	v_mul_f32_e32 v95, v65, v95
	v_fma_f32 v95, v65, v95, v65
	v_mul_f32_e32 v95, 0x3f4c422a, v95
	v_add_f32_e32 v95, v95, v95
	v_mul_f32_e32 v95, 0x3fb8aa3b, v95
	v_exp_f32_e32 v95, v95
	v_pk_mul_f32 v[64:65], v[64:65], 0.5 op_sel_hi:[1,0]
	v_mfma_f32_16x16x32_f16 v[4:7], v[250:253], v[100:103], v[4:7]
	v_add_f32_e32 v95, 1.0, v95
	v_rcp_f32_e32 v97, v95
	s_nop 0
	v_pk_fma_f32 v[96:97], v[96:97], 2.0, 1.0 op_sel_hi:[1,0,0] neg_lo:[1,0,0] neg_hi:[1,0,0]
	s_nop 0
	v_pk_add_f32 v[96:97], v[96:97], 1.0 op_sel_hi:[1,0]
	s_nop 0
	v_pk_mul_f32 v[64:65], v[64:65], v[96:97]
	s_nop 0
	v_cvt_pk_f16_f32 v64, v64, v65
	v_mul_f32_e32 v65, 0x3d372713, v66
	v_mul_f32_e32 v65, v66, v65
	v_fma_f32 v65, v66, v65, v66
	v_mul_f32_e32 v65, 0x3f4c422a, v65
	v_add_f32_e32 v65, v65, v65
	v_mul_f32_e32 v65, 0x3fb8aa3b, v65
	v_exp_f32_e32 v65, v65
	s_nop 0
	v_add_f32_e32 v65, 1.0, v65
	v_rcp_f32_e32 v96, v65
	v_mul_f32_e32 v65, 0x3d372713, v67
	v_mul_f32_e32 v65, v67, v65
	v_fma_f32 v65, v67, v65, v67
	v_mul_f32_e32 v65, 0x3f4c422a, v65
	v_add_f32_e32 v65, v65, v65
	v_mul_f32_e32 v65, 0x3fb8aa3b, v65
	v_exp_f32_e32 v65, v65
	v_pk_mul_f32 v[66:67], v[66:67], 0.5 op_sel_hi:[1,0]
	v_add_f32_e32 v65, 1.0, v65
	v_rcp_f32_e32 v97, v65
	s_nop 0
	v_pk_fma_f32 v[96:97], v[96:97], 2.0, 1.0 op_sel_hi:[1,0,0] neg_lo:[1,0,0] neg_hi:[1,0,0]
	s_nop 0
	v_pk_add_f32 v[96:97], v[96:97], 1.0 op_sel_hi:[1,0]
	s_nop 0
	v_pk_mul_f32 v[66:67], v[66:67], v[96:97]
	s_nop 0
	v_cvt_pk_f16_f32 v65, v66, v67
	v_lshlrev_b64 v[66:67], 11, v[88:89]
	v_mul_f32_e32 v88, 0x3d372713, v60
	v_mul_f32_e32 v89, 0x3d372713, v61
	v_mul_f32_e32 v88, v60, v88
	v_mul_f32_e32 v89, v61, v89
	v_fma_f32 v88, v60, v88, v60
	v_fma_f32 v89, v61, v89, v61
	v_mul_f32_e32 v88, 0x3f4c422a, v88
	v_mul_f32_e32 v89, 0x3f4c422a, v89
	v_add_f32_e32 v88, v88, v88
	v_add_f32_e32 v89, v89, v89
	v_mul_f32_e32 v88, 0x3fb8aa3b, v88
	v_mul_f32_e32 v89, 0x3fb8aa3b, v89
	v_exp_f32_e32 v88, v88
	v_exp_f32_e32 v89, v89
	v_pk_mul_f32 v[60:61], v[60:61], 0.5 op_sel_hi:[1,0]
	v_lshl_add_u64 v[66:67], v[68:69], 0, v[66:67]
	v_add_f32_e32 v88, 1.0, v88
	v_add_f32_e32 v89, 1.0, v89
	v_rcp_f32_e32 v88, v88
	v_rcp_f32_e32 v89, v89
	global_store_dwordx2 v[66:67], v[64:65], off
	v_or_b32_e32 v64, 0x400, v2
	v_mov_b32_e32 v65, v3
	v_pk_fma_f32 v[88:89], v[88:89], 2.0, 1.0 op_sel_hi:[1,0,0] neg_lo:[1,0,0] neg_hi:[1,0,0]
	v_lshl_add_u64 v[66:67], s[18:19], 0, v[64:65]
	v_pk_add_f32 v[88:89], v[88:89], 1.0 op_sel_hi:[1,0]
	s_nop 0
	v_pk_mul_f32 v[60:61], v[60:61], v[88:89]
	s_nop 0
	v_cvt_pk_f16_f32 v60, v60, v61
	v_mul_f32_e32 v61, 0x3d372713, v62
	v_mul_f32_e32 v61, v62, v61
	v_fma_f32 v61, v62, v61, v62
	v_mul_f32_e32 v61, 0x3f4c422a, v61
	v_add_f32_e32 v61, v61, v61
	v_mul_f32_e32 v61, 0x3fb8aa3b, v61
	v_exp_f32_e32 v61, v61
	s_nop 0
	v_add_f32_e32 v61, 1.0, v61
	v_rcp_f32_e32 v88, v61
	v_mul_f32_e32 v61, 0x3d372713, v63
	v_mul_f32_e32 v61, v63, v61
	v_fma_f32 v61, v63, v61, v63
	v_mul_f32_e32 v61, 0x3f4c422a, v61
	v_add_f32_e32 v61, v61, v61
	v_mul_f32_e32 v61, 0x3fb8aa3b, v61
	v_exp_f32_e32 v61, v61
	v_pk_mul_f32 v[62:63], v[62:63], 0.5 op_sel_hi:[1,0]
	v_add_f32_e32 v61, 1.0, v61
	v_rcp_f32_e32 v89, v61
	s_nop 0
	v_pk_fma_f32 v[88:89], v[88:89], 2.0, 1.0 op_sel_hi:[1,0,0] neg_lo:[1,0,0] neg_hi:[1,0,0]
	s_nop 0
	v_pk_add_f32 v[88:89], v[88:89], 1.0 op_sel_hi:[1,0]
	s_nop 0
	v_pk_mul_f32 v[62:63], v[62:63], v[88:89]
	s_nop 0
	v_cvt_pk_f16_f32 v61, v62, v63
	v_lshlrev_b64 v[62:63], 11, v[66:67]
	v_lshl_add_u64 v[62:63], v[68:69], 0, v[62:63]
	global_store_dwordx2 v[62:63], v[60:61], off
	v_mul_f32_e32 v62, 0x3d372713, v56
	v_mul_f32_e32 v63, 0x3d372713, v57
	v_mul_f32_e32 v62, v56, v62
	v_mul_f32_e32 v63, v57, v63
	v_fma_f32 v62, v56, v62, v56
	v_fma_f32 v63, v57, v63, v57
	v_mul_f32_e32 v62, 0x3f4c422a, v62
	v_mul_f32_e32 v63, 0x3f4c422a, v63
	v_add_f32_e32 v62, v62, v62
	v_add_f32_e32 v63, v63, v63
	v_mul_f32_e32 v62, 0x3fb8aa3b, v62
	v_mul_f32_e32 v63, 0x3fb8aa3b, v63
	v_exp_f32_e32 v62, v62
	v_exp_f32_e32 v63, v63
	v_pk_mul_f32 v[56:57], v[56:57], 0.5 op_sel_hi:[1,0]
	v_lshl_add_u64 v[60:61], s[20:21], 0, v[2:3]
	v_add_f32_e32 v62, 1.0, v62
	v_add_f32_e32 v63, 1.0, v63
	v_rcp_f32_e32 v62, v62
	v_rcp_f32_e32 v63, v63
	s_nop 0
	v_pk_fma_f32 v[62:63], v[62:63], 2.0, 1.0 op_sel_hi:[1,0,0] neg_lo:[1,0,0] neg_hi:[1,0,0]
	s_nop 0
	v_pk_add_f32 v[62:63], v[62:63], 1.0 op_sel_hi:[1,0]
	s_nop 0
	v_pk_mul_f32 v[56:57], v[56:57], v[62:63]
	s_nop 0
	v_cvt_pk_f16_f32 v56, v56, v57
	v_mul_f32_e32 v57, 0x3d372713, v58
	v_mul_f32_e32 v57, v58, v57
	v_fma_f32 v57, v58, v57, v58
	v_mul_f32_e32 v57, 0x3f4c422a, v57
	v_add_f32_e32 v57, v57, v57
	v_mul_f32_e32 v57, 0x3fb8aa3b, v57
	v_exp_f32_e32 v57, v57
	s_nop 0
	v_add_f32_e32 v57, 1.0, v57
	v_rcp_f32_e32 v62, v57
	v_mul_f32_e32 v57, 0x3d372713, v59
	v_mul_f32_e32 v57, v59, v57
	v_fma_f32 v57, v59, v57, v59
	v_mul_f32_e32 v57, 0x3f4c422a, v57
	v_add_f32_e32 v57, v57, v57
	v_mul_f32_e32 v57, 0x3fb8aa3b, v57
	v_exp_f32_e32 v57, v57
	v_pk_mul_f32 v[58:59], v[58:59], 0.5 op_sel_hi:[1,0]
	v_add_f32_e32 v57, 1.0, v57
	v_rcp_f32_e32 v63, v57
	s_nop 0
	v_pk_fma_f32 v[62:63], v[62:63], 2.0, 1.0 op_sel_hi:[1,0,0] neg_lo:[1,0,0] neg_hi:[1,0,0]
	s_nop 0
	v_pk_add_f32 v[62:63], v[62:63], 1.0 op_sel_hi:[1,0]
	s_nop 0
	v_pk_mul_f32 v[58:59], v[58:59], v[62:63]
	s_nop 0
	v_cvt_pk_f16_f32 v57, v58, v59
	v_lshlrev_b64 v[58:59], 11, v[60:61]
	v_lshl_add_u64 v[58:59], v[68:69], 0, v[58:59]
	global_store_dwordx2 v[58:59], v[56:57], off
	v_mul_f32_e32 v58, 0x3d372713, v52
	v_mul_f32_e32 v59, 0x3d372713, v53
	v_mul_f32_e32 v58, v52, v58
	v_mul_f32_e32 v59, v53, v59
	v_fma_f32 v58, v52, v58, v52
	v_fma_f32 v59, v53, v59, v53
	v_mul_f32_e32 v58, 0x3f4c422a, v58
	v_mul_f32_e32 v59, 0x3f4c422a, v59
	v_add_f32_e32 v58, v58, v58
	v_add_f32_e32 v59, v59, v59
	v_mul_f32_e32 v58, 0x3fb8aa3b, v58
	v_mul_f32_e32 v59, 0x3fb8aa3b, v59
	v_exp_f32_e32 v58, v58
	v_exp_f32_e32 v59, v59
	v_pk_mul_f32 v[52:53], v[52:53], 0.5 op_sel_hi:[1,0]
	v_lshl_add_u64 v[56:57], s[20:21], 0, v[64:65]
	v_add_f32_e32 v58, 1.0, v58
	v_add_f32_e32 v59, 1.0, v59
	v_rcp_f32_e32 v58, v58
	v_rcp_f32_e32 v59, v59
	s_nop 0
	v_pk_fma_f32 v[58:59], v[58:59], 2.0, 1.0 op_sel_hi:[1,0,0] neg_lo:[1,0,0] neg_hi:[1,0,0]
	s_nop 0
	v_pk_add_f32 v[58:59], v[58:59], 1.0 op_sel_hi:[1,0]
	s_nop 0
	v_pk_mul_f32 v[52:53], v[52:53], v[58:59]
	s_nop 0
	v_cvt_pk_f16_f32 v52, v52, v53
	v_mul_f32_e32 v53, 0x3d372713, v54
	v_mul_f32_e32 v53, v54, v53
	v_fma_f32 v53, v54, v53, v54
	v_mul_f32_e32 v53, 0x3f4c422a, v53
	v_add_f32_e32 v53, v53, v53
	v_mul_f32_e32 v53, 0x3fb8aa3b, v53
	v_exp_f32_e32 v53, v53
	s_nop 0
	v_add_f32_e32 v53, 1.0, v53
	v_rcp_f32_e32 v58, v53
	v_mul_f32_e32 v53, 0x3d372713, v55
	v_mul_f32_e32 v53, v55, v53
	v_fma_f32 v53, v55, v53, v55
	v_mul_f32_e32 v53, 0x3f4c422a, v53
	v_add_f32_e32 v53, v53, v53
	v_mul_f32_e32 v53, 0x3fb8aa3b, v53
	v_exp_f32_e32 v53, v53
	v_pk_mul_f32 v[54:55], v[54:55], 0.5 op_sel_hi:[1,0]
	v_add_f32_e32 v53, 1.0, v53
	v_rcp_f32_e32 v59, v53
	s_nop 0
	v_pk_fma_f32 v[58:59], v[58:59], 2.0, 1.0 op_sel_hi:[1,0,0] neg_lo:[1,0,0] neg_hi:[1,0,0]
	s_nop 0
	v_pk_add_f32 v[58:59], v[58:59], 1.0 op_sel_hi:[1,0]
	s_nop 0
	v_pk_mul_f32 v[54:55], v[54:55], v[58:59]
	s_nop 0
	v_cvt_pk_f16_f32 v53, v54, v55
	v_lshlrev_b64 v[54:55], 11, v[56:57]
	v_lshl_add_u64 v[54:55], v[68:69], 0, v[54:55]
	global_store_dwordx2 v[54:55], v[52:53], off
	v_mul_f32_e32 v54, 0x3d372713, v48
	v_mul_f32_e32 v55, 0x3d372713, v49
	v_mul_f32_e32 v54, v48, v54
	v_mul_f32_e32 v55, v49, v55
	v_fma_f32 v54, v48, v54, v48
	v_fma_f32 v55, v49, v55, v49
	v_mul_f32_e32 v54, 0x3f4c422a, v54
	v_mul_f32_e32 v55, 0x3f4c422a, v55
	v_add_f32_e32 v54, v54, v54
	v_add_f32_e32 v55, v55, v55
	v_mul_f32_e32 v54, 0x3fb8aa3b, v54
	v_mul_f32_e32 v55, 0x3fb8aa3b, v55
	v_exp_f32_e32 v54, v54
	v_exp_f32_e32 v55, v55
	v_pk_mul_f32 v[48:49], v[48:49], 0.5 op_sel_hi:[1,0]
	v_lshl_add_u64 v[52:53], s[22:23], 0, v[2:3]
	v_add_f32_e32 v54, 1.0, v54
	v_add_f32_e32 v55, 1.0, v55
	v_rcp_f32_e32 v54, v54
	v_rcp_f32_e32 v55, v55
	s_nop 0
	v_pk_fma_f32 v[54:55], v[54:55], 2.0, 1.0 op_sel_hi:[1,0,0] neg_lo:[1,0,0] neg_hi:[1,0,0]
	s_nop 0
	v_pk_add_f32 v[54:55], v[54:55], 1.0 op_sel_hi:[1,0]
	s_nop 0
	v_pk_mul_f32 v[48:49], v[48:49], v[54:55]
	s_nop 0
	v_cvt_pk_f16_f32 v48, v48, v49
	v_mul_f32_e32 v49, 0x3d372713, v50
	v_mul_f32_e32 v49, v50, v49
	v_fma_f32 v49, v50, v49, v50
	v_mul_f32_e32 v49, 0x3f4c422a, v49
	v_add_f32_e32 v49, v49, v49
	v_mul_f32_e32 v49, 0x3fb8aa3b, v49
	v_exp_f32_e32 v49, v49
	s_nop 0
	v_add_f32_e32 v49, 1.0, v49
	v_rcp_f32_e32 v54, v49
	v_mul_f32_e32 v49, 0x3d372713, v51
	v_mul_f32_e32 v49, v51, v49
	v_fma_f32 v49, v51, v49, v51
	v_mul_f32_e32 v49, 0x3f4c422a, v49
	v_add_f32_e32 v49, v49, v49
	v_mul_f32_e32 v49, 0x3fb8aa3b, v49
	v_exp_f32_e32 v49, v49
	v_pk_mul_f32 v[50:51], v[50:51], 0.5 op_sel_hi:[1,0]
	v_add_f32_e32 v49, 1.0, v49
	v_rcp_f32_e32 v55, v49
	s_nop 0
	v_pk_fma_f32 v[54:55], v[54:55], 2.0, 1.0 op_sel_hi:[1,0,0] neg_lo:[1,0,0] neg_hi:[1,0,0]
	s_nop 0
	v_pk_add_f32 v[54:55], v[54:55], 1.0 op_sel_hi:[1,0]
	s_nop 0
	v_pk_mul_f32 v[50:51], v[50:51], v[54:55]
	s_nop 0
	v_cvt_pk_f16_f32 v49, v50, v51
	v_lshlrev_b64 v[50:51], 11, v[52:53]
	v_lshl_add_u64 v[50:51], v[68:69], 0, v[50:51]
	global_store_dwordx2 v[50:51], v[48:49], off
	v_mul_f32_e32 v50, 0x3d372713, v44
	v_mul_f32_e32 v51, 0x3d372713, v45
	v_mul_f32_e32 v50, v44, v50
	v_mul_f32_e32 v51, v45, v51
	v_fma_f32 v50, v44, v50, v44
	v_fma_f32 v51, v45, v51, v45
	v_mul_f32_e32 v50, 0x3f4c422a, v50
	v_mul_f32_e32 v51, 0x3f4c422a, v51
	v_add_f32_e32 v50, v50, v50
	v_add_f32_e32 v51, v51, v51
	v_mul_f32_e32 v50, 0x3fb8aa3b, v50
	v_mul_f32_e32 v51, 0x3fb8aa3b, v51
	v_exp_f32_e32 v50, v50
	v_exp_f32_e32 v51, v51
	v_pk_mul_f32 v[44:45], v[44:45], 0.5 op_sel_hi:[1,0]
	v_lshl_add_u64 v[48:49], s[22:23], 0, v[64:65]
	v_add_f32_e32 v50, 1.0, v50
	v_add_f32_e32 v51, 1.0, v51
	v_rcp_f32_e32 v50, v50
	v_rcp_f32_e32 v51, v51
	s_nop 0
	v_pk_fma_f32 v[50:51], v[50:51], 2.0, 1.0 op_sel_hi:[1,0,0] neg_lo:[1,0,0] neg_hi:[1,0,0]
	s_nop 0
	v_pk_add_f32 v[50:51], v[50:51], 1.0 op_sel_hi:[1,0]
	s_nop 0
	v_pk_mul_f32 v[44:45], v[44:45], v[50:51]
	s_nop 0
	v_cvt_pk_f16_f32 v44, v44, v45
	v_mul_f32_e32 v45, 0x3d372713, v46
	v_mul_f32_e32 v45, v46, v45
	v_fma_f32 v45, v46, v45, v46
	v_mul_f32_e32 v45, 0x3f4c422a, v45
	v_add_f32_e32 v45, v45, v45
	v_mul_f32_e32 v45, 0x3fb8aa3b, v45
	v_exp_f32_e32 v45, v45
	s_nop 0
	v_add_f32_e32 v45, 1.0, v45
	v_rcp_f32_e32 v50, v45
	v_mul_f32_e32 v45, 0x3d372713, v47
	v_mul_f32_e32 v45, v47, v45
	v_fma_f32 v45, v47, v45, v47
	v_mul_f32_e32 v45, 0x3f4c422a, v45
	v_add_f32_e32 v45, v45, v45
	v_mul_f32_e32 v45, 0x3fb8aa3b, v45
	v_exp_f32_e32 v45, v45
	v_pk_mul_f32 v[46:47], v[46:47], 0.5 op_sel_hi:[1,0]
	v_add_f32_e32 v45, 1.0, v45
	v_rcp_f32_e32 v51, v45
	s_nop 0
	v_pk_fma_f32 v[50:51], v[50:51], 2.0, 1.0 op_sel_hi:[1,0,0] neg_lo:[1,0,0] neg_hi:[1,0,0]
	s_nop 0
	v_pk_add_f32 v[50:51], v[50:51], 1.0 op_sel_hi:[1,0]
	s_nop 0
	v_pk_mul_f32 v[46:47], v[46:47], v[50:51]
	s_nop 0
	v_cvt_pk_f16_f32 v45, v46, v47
	v_lshlrev_b64 v[46:47], 11, v[48:49]
	v_lshl_add_u64 v[46:47], v[68:69], 0, v[46:47]
	global_store_dwordx2 v[46:47], v[44:45], off
	v_mul_f32_e32 v46, 0x3d372713, v40
	v_mul_f32_e32 v47, 0x3d372713, v41
	v_mul_f32_e32 v46, v40, v46
	v_mul_f32_e32 v47, v41, v47
	v_fma_f32 v46, v40, v46, v40
	v_fma_f32 v47, v41, v47, v41
	v_mul_f32_e32 v46, 0x3f4c422a, v46
	v_mul_f32_e32 v47, 0x3f4c422a, v47
	v_add_f32_e32 v46, v46, v46
	v_add_f32_e32 v47, v47, v47
	v_mul_f32_e32 v46, 0x3fb8aa3b, v46
	v_mul_f32_e32 v47, 0x3fb8aa3b, v47
	v_exp_f32_e32 v46, v46
	v_exp_f32_e32 v47, v47
	v_pk_mul_f32 v[40:41], v[40:41], 0.5 op_sel_hi:[1,0]
	v_lshl_add_u64 v[44:45], s[24:25], 0, v[2:3]
	v_add_f32_e32 v46, 1.0, v46
	v_add_f32_e32 v47, 1.0, v47
	v_rcp_f32_e32 v46, v46
	v_rcp_f32_e32 v47, v47
	s_nop 0
	v_pk_fma_f32 v[46:47], v[46:47], 2.0, 1.0 op_sel_hi:[1,0,0] neg_lo:[1,0,0] neg_hi:[1,0,0]
	s_nop 0
	v_pk_add_f32 v[46:47], v[46:47], 1.0 op_sel_hi:[1,0]
	s_nop 0
	v_pk_mul_f32 v[40:41], v[40:41], v[46:47]
	s_nop 0
	v_cvt_pk_f16_f32 v40, v40, v41
	v_mul_f32_e32 v41, 0x3d372713, v42
	v_mul_f32_e32 v41, v42, v41
	v_fma_f32 v41, v42, v41, v42
	v_mul_f32_e32 v41, 0x3f4c422a, v41
	v_add_f32_e32 v41, v41, v41
	v_mul_f32_e32 v41, 0x3fb8aa3b, v41
	v_exp_f32_e32 v41, v41
	s_nop 0
	v_add_f32_e32 v41, 1.0, v41
	v_rcp_f32_e32 v46, v41
	v_mul_f32_e32 v41, 0x3d372713, v43
	v_mul_f32_e32 v41, v43, v41
	v_fma_f32 v41, v43, v41, v43
	v_mul_f32_e32 v41, 0x3f4c422a, v41
	v_add_f32_e32 v41, v41, v41
	v_mul_f32_e32 v41, 0x3fb8aa3b, v41
	v_exp_f32_e32 v41, v41
	v_pk_mul_f32 v[42:43], v[42:43], 0.5 op_sel_hi:[1,0]
	v_add_f32_e32 v41, 1.0, v41
	v_rcp_f32_e32 v47, v41
	s_nop 0
	v_pk_fma_f32 v[46:47], v[46:47], 2.0, 1.0 op_sel_hi:[1,0,0] neg_lo:[1,0,0] neg_hi:[1,0,0]
	s_nop 0
	v_pk_add_f32 v[46:47], v[46:47], 1.0 op_sel_hi:[1,0]
	s_nop 0
	v_pk_mul_f32 v[42:43], v[42:43], v[46:47]
	s_nop 0
	v_cvt_pk_f16_f32 v41, v42, v43
	v_lshlrev_b64 v[42:43], 11, v[44:45]
	v_lshl_add_u64 v[42:43], v[68:69], 0, v[42:43]
	global_store_dwordx2 v[42:43], v[40:41], off
	v_mul_f32_e32 v42, 0x3d372713, v36
	v_mul_f32_e32 v43, 0x3d372713, v37
	v_mul_f32_e32 v42, v36, v42
	v_mul_f32_e32 v43, v37, v43
	v_fma_f32 v42, v36, v42, v36
	v_fma_f32 v43, v37, v43, v37
	v_mul_f32_e32 v42, 0x3f4c422a, v42
	v_mul_f32_e32 v43, 0x3f4c422a, v43
	v_add_f32_e32 v42, v42, v42
	v_add_f32_e32 v43, v43, v43
	v_mul_f32_e32 v42, 0x3fb8aa3b, v42
	v_mul_f32_e32 v43, 0x3fb8aa3b, v43
	v_exp_f32_e32 v42, v42
	v_exp_f32_e32 v43, v43
	v_pk_mul_f32 v[36:37], v[36:37], 0.5 op_sel_hi:[1,0]
	v_lshl_add_u64 v[40:41], s[24:25], 0, v[64:65]
	v_add_f32_e32 v42, 1.0, v42
	v_add_f32_e32 v43, 1.0, v43
	v_rcp_f32_e32 v42, v42
	v_rcp_f32_e32 v43, v43
	s_nop 0
	v_pk_fma_f32 v[42:43], v[42:43], 2.0, 1.0 op_sel_hi:[1,0,0] neg_lo:[1,0,0] neg_hi:[1,0,0]
	s_nop 0
	v_pk_add_f32 v[42:43], v[42:43], 1.0 op_sel_hi:[1,0]
	s_nop 0
	v_pk_mul_f32 v[36:37], v[36:37], v[42:43]
	s_nop 0
	v_cvt_pk_f16_f32 v36, v36, v37
	v_mul_f32_e32 v37, 0x3d372713, v38
	v_mul_f32_e32 v37, v38, v37
	v_fma_f32 v37, v38, v37, v38
	v_mul_f32_e32 v37, 0x3f4c422a, v37
	v_add_f32_e32 v37, v37, v37
	v_mul_f32_e32 v37, 0x3fb8aa3b, v37
	v_exp_f32_e32 v37, v37
	s_nop 0
	v_add_f32_e32 v37, 1.0, v37
	v_rcp_f32_e32 v42, v37
	v_mul_f32_e32 v37, 0x3d372713, v39
	v_mul_f32_e32 v37, v39, v37
	v_fma_f32 v37, v39, v37, v39
	v_mul_f32_e32 v37, 0x3f4c422a, v37
	v_add_f32_e32 v37, v37, v37
	v_mul_f32_e32 v37, 0x3fb8aa3b, v37
	v_exp_f32_e32 v37, v37
	v_pk_mul_f32 v[38:39], v[38:39], 0.5 op_sel_hi:[1,0]
	v_add_f32_e32 v37, 1.0, v37
	v_rcp_f32_e32 v43, v37
	s_nop 0
	v_pk_fma_f32 v[42:43], v[42:43], 2.0, 1.0 op_sel_hi:[1,0,0] neg_lo:[1,0,0] neg_hi:[1,0,0]
	s_nop 0
	v_pk_add_f32 v[42:43], v[42:43], 1.0 op_sel_hi:[1,0]
	s_nop 0
	v_pk_mul_f32 v[38:39], v[38:39], v[42:43]
	s_nop 0
	v_cvt_pk_f16_f32 v37, v38, v39
	v_lshlrev_b64 v[38:39], 11, v[40:41]
	v_lshl_add_u64 v[38:39], v[68:69], 0, v[38:39]
	global_store_dwordx2 v[38:39], v[36:37], off
	v_mul_f32_e32 v38, 0x3d372713, v32
	v_mul_f32_e32 v39, 0x3d372713, v33
	v_mul_f32_e32 v38, v32, v38
	v_mul_f32_e32 v39, v33, v39
	v_fma_f32 v38, v32, v38, v32
	v_fma_f32 v39, v33, v39, v33
	v_mul_f32_e32 v38, 0x3f4c422a, v38
	v_mul_f32_e32 v39, 0x3f4c422a, v39
	v_add_f32_e32 v38, v38, v38
	v_add_f32_e32 v39, v39, v39
	v_mul_f32_e32 v38, 0x3fb8aa3b, v38
	v_mul_f32_e32 v39, 0x3fb8aa3b, v39
	v_exp_f32_e32 v38, v38
	v_exp_f32_e32 v39, v39
	v_pk_mul_f32 v[32:33], v[32:33], 0.5 op_sel_hi:[1,0]
	v_lshl_add_u64 v[36:37], s[26:27], 0, v[2:3]
	v_add_f32_e32 v38, 1.0, v38
	v_add_f32_e32 v39, 1.0, v39
	v_rcp_f32_e32 v38, v38
	v_rcp_f32_e32 v39, v39
	s_nop 0
	v_pk_fma_f32 v[38:39], v[38:39], 2.0, 1.0 op_sel_hi:[1,0,0] neg_lo:[1,0,0] neg_hi:[1,0,0]
	s_nop 0
	v_pk_add_f32 v[38:39], v[38:39], 1.0 op_sel_hi:[1,0]
	s_nop 0
	v_pk_mul_f32 v[32:33], v[32:33], v[38:39]
	s_nop 0
	v_cvt_pk_f16_f32 v32, v32, v33
	v_mul_f32_e32 v33, 0x3d372713, v34
	v_mul_f32_e32 v33, v34, v33
	v_fma_f32 v33, v34, v33, v34
	v_mul_f32_e32 v33, 0x3f4c422a, v33
	v_add_f32_e32 v33, v33, v33
	v_mul_f32_e32 v33, 0x3fb8aa3b, v33
	v_exp_f32_e32 v33, v33
	s_nop 0
	v_add_f32_e32 v33, 1.0, v33
	v_rcp_f32_e32 v38, v33
	v_mul_f32_e32 v33, 0x3d372713, v35
	v_mul_f32_e32 v33, v35, v33
	v_fma_f32 v33, v35, v33, v35
	v_mul_f32_e32 v33, 0x3f4c422a, v33
	v_add_f32_e32 v33, v33, v33
	v_mul_f32_e32 v33, 0x3fb8aa3b, v33
	v_exp_f32_e32 v33, v33
	v_pk_mul_f32 v[34:35], v[34:35], 0.5 op_sel_hi:[1,0]
	v_add_f32_e32 v33, 1.0, v33
	v_rcp_f32_e32 v39, v33
	s_nop 0
	v_pk_fma_f32 v[38:39], v[38:39], 2.0, 1.0 op_sel_hi:[1,0,0] neg_lo:[1,0,0] neg_hi:[1,0,0]
	s_nop 0
	v_pk_add_f32 v[38:39], v[38:39], 1.0 op_sel_hi:[1,0]
	s_nop 0
	v_pk_mul_f32 v[34:35], v[34:35], v[38:39]
	s_nop 0
	v_cvt_pk_f16_f32 v33, v34, v35
	v_lshlrev_b64 v[34:35], 11, v[36:37]
	v_lshl_add_u64 v[34:35], v[68:69], 0, v[34:35]
	global_store_dwordx2 v[34:35], v[32:33], off
	v_mul_f32_e32 v34, 0x3d372713, v28
	v_mul_f32_e32 v35, 0x3d372713, v29
	v_mul_f32_e32 v34, v28, v34
	v_mul_f32_e32 v35, v29, v35
	v_fma_f32 v34, v28, v34, v28
	v_fma_f32 v35, v29, v35, v29
	v_mul_f32_e32 v34, 0x3f4c422a, v34
	v_mul_f32_e32 v35, 0x3f4c422a, v35
	v_add_f32_e32 v34, v34, v34
	v_add_f32_e32 v35, v35, v35
	v_mul_f32_e32 v34, 0x3fb8aa3b, v34
	v_mul_f32_e32 v35, 0x3fb8aa3b, v35
	v_exp_f32_e32 v34, v34
	v_exp_f32_e32 v35, v35
	v_pk_mul_f32 v[28:29], v[28:29], 0.5 op_sel_hi:[1,0]
	v_lshl_add_u64 v[32:33], s[26:27], 0, v[64:65]
	v_add_f32_e32 v34, 1.0, v34
	v_add_f32_e32 v35, 1.0, v35
	v_rcp_f32_e32 v34, v34
	v_rcp_f32_e32 v35, v35
	s_nop 0
	v_pk_fma_f32 v[34:35], v[34:35], 2.0, 1.0 op_sel_hi:[1,0,0] neg_lo:[1,0,0] neg_hi:[1,0,0]
	s_nop 0
	v_pk_add_f32 v[34:35], v[34:35], 1.0 op_sel_hi:[1,0]
	s_nop 0
	v_pk_mul_f32 v[28:29], v[28:29], v[34:35]
	s_nop 0
	v_cvt_pk_f16_f32 v28, v28, v29
	v_mul_f32_e32 v29, 0x3d372713, v30
	v_mul_f32_e32 v29, v30, v29
	v_fma_f32 v29, v30, v29, v30
	v_mul_f32_e32 v29, 0x3f4c422a, v29
	v_add_f32_e32 v29, v29, v29
	v_mul_f32_e32 v29, 0x3fb8aa3b, v29
	v_exp_f32_e32 v29, v29
	s_nop 0
	v_add_f32_e32 v29, 1.0, v29
	v_rcp_f32_e32 v34, v29
	v_mul_f32_e32 v29, 0x3d372713, v31
	v_mul_f32_e32 v29, v31, v29
	v_fma_f32 v29, v31, v29, v31
	v_mul_f32_e32 v29, 0x3f4c422a, v29
	v_add_f32_e32 v29, v29, v29
	v_mul_f32_e32 v29, 0x3fb8aa3b, v29
	v_exp_f32_e32 v29, v29
	v_pk_mul_f32 v[30:31], v[30:31], 0.5 op_sel_hi:[1,0]
	v_add_f32_e32 v29, 1.0, v29
	v_rcp_f32_e32 v35, v29
	s_nop 0
	v_pk_fma_f32 v[34:35], v[34:35], 2.0, 1.0 op_sel_hi:[1,0,0] neg_lo:[1,0,0] neg_hi:[1,0,0]
	s_nop 0
	v_pk_add_f32 v[34:35], v[34:35], 1.0 op_sel_hi:[1,0]
	s_nop 0
	v_pk_mul_f32 v[30:31], v[30:31], v[34:35]
	s_nop 0
	v_cvt_pk_f16_f32 v29, v30, v31
	v_lshlrev_b64 v[30:31], 11, v[32:33]
	v_lshl_add_u64 v[30:31], v[68:69], 0, v[30:31]
	global_store_dwordx2 v[30:31], v[28:29], off
	v_mul_f32_e32 v30, 0x3d372713, v24
	v_mul_f32_e32 v31, 0x3d372713, v25
	v_mul_f32_e32 v30, v24, v30
	v_mul_f32_e32 v31, v25, v31
	v_fma_f32 v30, v24, v30, v24
	v_fma_f32 v31, v25, v31, v25
	v_mul_f32_e32 v30, 0x3f4c422a, v30
	v_mul_f32_e32 v31, 0x3f4c422a, v31
	v_add_f32_e32 v30, v30, v30
	v_add_f32_e32 v31, v31, v31
	v_mul_f32_e32 v30, 0x3fb8aa3b, v30
	v_mul_f32_e32 v31, 0x3fb8aa3b, v31
	v_exp_f32_e32 v30, v30
	v_exp_f32_e32 v31, v31
	v_pk_mul_f32 v[24:25], v[24:25], 0.5 op_sel_hi:[1,0]
	v_lshl_add_u64 v[28:29], s[28:29], 0, v[2:3]
	v_add_f32_e32 v30, 1.0, v30
	v_add_f32_e32 v31, 1.0, v31
	v_rcp_f32_e32 v30, v30
	v_rcp_f32_e32 v31, v31
	s_nop 0
	v_pk_fma_f32 v[30:31], v[30:31], 2.0, 1.0 op_sel_hi:[1,0,0] neg_lo:[1,0,0] neg_hi:[1,0,0]
	s_nop 0
	v_pk_add_f32 v[30:31], v[30:31], 1.0 op_sel_hi:[1,0]
	s_nop 0
	v_pk_mul_f32 v[24:25], v[24:25], v[30:31]
	s_nop 0
	v_cvt_pk_f16_f32 v24, v24, v25
	v_mul_f32_e32 v25, 0x3d372713, v26
	v_mul_f32_e32 v25, v26, v25
	v_fma_f32 v25, v26, v25, v26
	v_mul_f32_e32 v25, 0x3f4c422a, v25
	v_add_f32_e32 v25, v25, v25
	v_mul_f32_e32 v25, 0x3fb8aa3b, v25
	v_exp_f32_e32 v25, v25
	s_nop 0
	v_add_f32_e32 v25, 1.0, v25
	v_rcp_f32_e32 v30, v25
	v_mul_f32_e32 v25, 0x3d372713, v27
	v_mul_f32_e32 v25, v27, v25
	v_fma_f32 v25, v27, v25, v27
	v_mul_f32_e32 v25, 0x3f4c422a, v25
	v_add_f32_e32 v25, v25, v25
	v_mul_f32_e32 v25, 0x3fb8aa3b, v25
	v_exp_f32_e32 v25, v25
	v_pk_mul_f32 v[26:27], v[26:27], 0.5 op_sel_hi:[1,0]
	v_add_f32_e32 v25, 1.0, v25
	v_rcp_f32_e32 v31, v25
	s_nop 0
	v_pk_fma_f32 v[30:31], v[30:31], 2.0, 1.0 op_sel_hi:[1,0,0] neg_lo:[1,0,0] neg_hi:[1,0,0]
	s_nop 0
	v_pk_add_f32 v[30:31], v[30:31], 1.0 op_sel_hi:[1,0]
	s_nop 0
	v_pk_mul_f32 v[26:27], v[26:27], v[30:31]
	s_nop 0
	v_cvt_pk_f16_f32 v25, v26, v27
	v_lshlrev_b64 v[26:27], 11, v[28:29]
	v_lshl_add_u64 v[26:27], v[68:69], 0, v[26:27]
	global_store_dwordx2 v[26:27], v[24:25], off
	v_mul_f32_e32 v26, 0x3d372713, v20
	v_mul_f32_e32 v27, 0x3d372713, v21
	v_mul_f32_e32 v26, v20, v26
	v_mul_f32_e32 v27, v21, v27
	v_fma_f32 v26, v20, v26, v20
	v_fma_f32 v27, v21, v27, v21
	v_mul_f32_e32 v26, 0x3f4c422a, v26
	v_mul_f32_e32 v27, 0x3f4c422a, v27
	v_add_f32_e32 v26, v26, v26
	v_add_f32_e32 v27, v27, v27
	v_mul_f32_e32 v26, 0x3fb8aa3b, v26
	v_mul_f32_e32 v27, 0x3fb8aa3b, v27
	v_exp_f32_e32 v26, v26
	v_exp_f32_e32 v27, v27
	v_pk_mul_f32 v[20:21], v[20:21], 0.5 op_sel_hi:[1,0]
	v_lshl_add_u64 v[24:25], s[28:29], 0, v[64:65]
	v_add_f32_e32 v26, 1.0, v26
	v_add_f32_e32 v27, 1.0, v27
	v_rcp_f32_e32 v26, v26
	v_rcp_f32_e32 v27, v27
	s_nop 0
	v_pk_fma_f32 v[26:27], v[26:27], 2.0, 1.0 op_sel_hi:[1,0,0] neg_lo:[1,0,0] neg_hi:[1,0,0]
	s_nop 0
	v_pk_add_f32 v[26:27], v[26:27], 1.0 op_sel_hi:[1,0]
	s_nop 0
	v_pk_mul_f32 v[20:21], v[20:21], v[26:27]
	s_nop 0
	v_cvt_pk_f16_f32 v20, v20, v21
	v_mul_f32_e32 v21, 0x3d372713, v22
	v_mul_f32_e32 v21, v22, v21
	v_fma_f32 v21, v22, v21, v22
	v_mul_f32_e32 v21, 0x3f4c422a, v21
	v_add_f32_e32 v21, v21, v21
	v_mul_f32_e32 v21, 0x3fb8aa3b, v21
	v_exp_f32_e32 v21, v21
	s_nop 0
	v_add_f32_e32 v21, 1.0, v21
	v_rcp_f32_e32 v26, v21
	v_mul_f32_e32 v21, 0x3d372713, v23
	v_mul_f32_e32 v21, v23, v21
	v_fma_f32 v21, v23, v21, v23
	v_mul_f32_e32 v21, 0x3f4c422a, v21
	v_add_f32_e32 v21, v21, v21
	v_mul_f32_e32 v21, 0x3fb8aa3b, v21
	v_exp_f32_e32 v21, v21
	v_pk_mul_f32 v[22:23], v[22:23], 0.5 op_sel_hi:[1,0]
	v_add_f32_e32 v21, 1.0, v21
	v_rcp_f32_e32 v27, v21
	s_nop 0
	v_pk_fma_f32 v[26:27], v[26:27], 2.0, 1.0 op_sel_hi:[1,0,0] neg_lo:[1,0,0] neg_hi:[1,0,0]
	s_nop 0
	v_pk_add_f32 v[26:27], v[26:27], 1.0 op_sel_hi:[1,0]
	s_nop 0
	v_pk_mul_f32 v[22:23], v[22:23], v[26:27]
	s_nop 0
	v_cvt_pk_f16_f32 v21, v22, v23
	v_lshlrev_b64 v[22:23], 11, v[24:25]
	v_lshl_add_u64 v[22:23], v[68:69], 0, v[22:23]
	global_store_dwordx2 v[22:23], v[20:21], off
	v_mul_f32_e32 v22, 0x3d372713, v16
	v_mul_f32_e32 v23, 0x3d372713, v17
	v_mul_f32_e32 v22, v16, v22
	v_mul_f32_e32 v23, v17, v23
	v_fma_f32 v22, v16, v22, v16
	v_fma_f32 v23, v17, v23, v17
	v_mul_f32_e32 v22, 0x3f4c422a, v22
	v_mul_f32_e32 v23, 0x3f4c422a, v23
	v_add_f32_e32 v22, v22, v22
	v_add_f32_e32 v23, v23, v23
	v_mul_f32_e32 v22, 0x3fb8aa3b, v22
	v_mul_f32_e32 v23, 0x3fb8aa3b, v23
	v_exp_f32_e32 v22, v22
	v_exp_f32_e32 v23, v23
	v_pk_mul_f32 v[16:17], v[16:17], 0.5 op_sel_hi:[1,0]
	v_lshl_add_u64 v[20:21], s[30:31], 0, v[2:3]
	v_add_f32_e32 v22, 1.0, v22
	v_add_f32_e32 v23, 1.0, v23
	v_rcp_f32_e32 v22, v22
	v_rcp_f32_e32 v23, v23
	s_nop 0
	v_pk_fma_f32 v[22:23], v[22:23], 2.0, 1.0 op_sel_hi:[1,0,0] neg_lo:[1,0,0] neg_hi:[1,0,0]
	s_nop 0
	v_pk_add_f32 v[22:23], v[22:23], 1.0 op_sel_hi:[1,0]
	s_nop 0
	v_pk_mul_f32 v[16:17], v[16:17], v[22:23]
	s_nop 0
	v_cvt_pk_f16_f32 v16, v16, v17
	v_mul_f32_e32 v17, 0x3d372713, v18
	v_mul_f32_e32 v17, v18, v17
	v_fma_f32 v17, v18, v17, v18
	v_mul_f32_e32 v17, 0x3f4c422a, v17
	v_add_f32_e32 v17, v17, v17
	v_mul_f32_e32 v17, 0x3fb8aa3b, v17
	v_exp_f32_e32 v17, v17
	s_nop 0
	v_add_f32_e32 v17, 1.0, v17
	v_rcp_f32_e32 v22, v17
	v_mul_f32_e32 v17, 0x3d372713, v19
	v_mul_f32_e32 v17, v19, v17
	v_fma_f32 v17, v19, v17, v19
	v_mul_f32_e32 v17, 0x3f4c422a, v17
	v_add_f32_e32 v17, v17, v17
	v_mul_f32_e32 v17, 0x3fb8aa3b, v17
	v_exp_f32_e32 v17, v17
	v_pk_mul_f32 v[18:19], v[18:19], 0.5 op_sel_hi:[1,0]
	v_add_f32_e32 v17, 1.0, v17
	v_rcp_f32_e32 v23, v17
	s_nop 0
	v_pk_fma_f32 v[22:23], v[22:23], 2.0, 1.0 op_sel_hi:[1,0,0] neg_lo:[1,0,0] neg_hi:[1,0,0]
	s_nop 0
	v_pk_add_f32 v[22:23], v[22:23], 1.0 op_sel_hi:[1,0]
	s_nop 0
	v_pk_mul_f32 v[18:19], v[18:19], v[22:23]
	s_nop 0
	v_cvt_pk_f16_f32 v17, v18, v19
	v_lshlrev_b64 v[18:19], 11, v[20:21]
	v_lshl_add_u64 v[18:19], v[68:69], 0, v[18:19]
	global_store_dwordx2 v[18:19], v[16:17], off
	v_mul_f32_e32 v18, 0x3d372713, v12
	v_mul_f32_e32 v19, 0x3d372713, v13
	v_mul_f32_e32 v18, v12, v18
	v_mul_f32_e32 v19, v13, v19
	v_fma_f32 v18, v12, v18, v12
	v_fma_f32 v19, v13, v19, v13
	v_mul_f32_e32 v18, 0x3f4c422a, v18
	v_mul_f32_e32 v19, 0x3f4c422a, v19
	v_add_f32_e32 v18, v18, v18
	v_add_f32_e32 v19, v19, v19
	v_mul_f32_e32 v18, 0x3fb8aa3b, v18
	v_mul_f32_e32 v19, 0x3fb8aa3b, v19
	v_exp_f32_e32 v18, v18
	v_exp_f32_e32 v19, v19
	v_pk_mul_f32 v[12:13], v[12:13], 0.5 op_sel_hi:[1,0]
	v_lshl_add_u64 v[16:17], s[30:31], 0, v[64:65]
	v_add_f32_e32 v18, 1.0, v18
	v_add_f32_e32 v19, 1.0, v19
	v_rcp_f32_e32 v18, v18
	v_rcp_f32_e32 v19, v19
	s_nop 0
	v_pk_fma_f32 v[18:19], v[18:19], 2.0, 1.0 op_sel_hi:[1,0,0] neg_lo:[1,0,0] neg_hi:[1,0,0]
	s_nop 0
	v_pk_add_f32 v[18:19], v[18:19], 1.0 op_sel_hi:[1,0]
	s_nop 0
	v_pk_mul_f32 v[12:13], v[12:13], v[18:19]
	s_nop 0
	v_cvt_pk_f16_f32 v12, v12, v13
	v_mul_f32_e32 v13, 0x3d372713, v14
	v_mul_f32_e32 v13, v14, v13
	v_fma_f32 v13, v14, v13, v14
	v_mul_f32_e32 v13, 0x3f4c422a, v13
	v_add_f32_e32 v13, v13, v13
	v_mul_f32_e32 v13, 0x3fb8aa3b, v13
	v_exp_f32_e32 v13, v13
	s_nop 0
	v_add_f32_e32 v13, 1.0, v13
	v_rcp_f32_e32 v18, v13
	v_mul_f32_e32 v13, 0x3d372713, v15
	v_mul_f32_e32 v13, v15, v13
	v_fma_f32 v13, v15, v13, v15
	v_mul_f32_e32 v13, 0x3f4c422a, v13
	v_add_f32_e32 v13, v13, v13
	v_mul_f32_e32 v13, 0x3fb8aa3b, v13
	v_exp_f32_e32 v13, v13
	v_pk_mul_f32 v[14:15], v[14:15], 0.5 op_sel_hi:[1,0]
	v_add_f32_e32 v13, 1.0, v13
	v_rcp_f32_e32 v19, v13
	s_nop 0
	v_pk_fma_f32 v[18:19], v[18:19], 2.0, 1.0 op_sel_hi:[1,0,0] neg_lo:[1,0,0] neg_hi:[1,0,0]
	s_nop 0
	v_pk_add_f32 v[18:19], v[18:19], 1.0 op_sel_hi:[1,0]
	s_nop 0
	v_pk_mul_f32 v[14:15], v[14:15], v[18:19]
	s_nop 0
	v_cvt_pk_f16_f32 v13, v14, v15
	v_lshlrev_b64 v[14:15], 11, v[16:17]
	v_lshl_add_u64 v[14:15], v[68:69], 0, v[14:15]
	global_store_dwordx2 v[14:15], v[12:13], off
	v_lshl_add_u64 v[12:13], s[16:17], 0, v[2:3]
	v_mul_f32_e32 v2, 0x3d372713, v8
	v_mul_f32_e32 v2, v8, v2
	v_fma_f32 v2, v8, v2, v8
	v_mul_f32_e32 v2, 0x3f4c422a, v2
	v_add_f32_e32 v2, v2, v2
	v_mul_f32_e32 v2, 0x3fb8aa3b, v2
	v_exp_f32_e32 v2, v2
	s_nop 0
	v_add_f32_e32 v2, 1.0, v2
	v_rcp_f32_e32 v14, v2
	v_mul_f32_e32 v2, 0x3d372713, v9
	v_mul_f32_e32 v2, v9, v2
	v_fma_f32 v2, v9, v2, v9
	v_mul_f32_e32 v2, 0x3f4c422a, v2
	v_add_f32_e32 v2, v2, v2
	v_mul_f32_e32 v2, 0x3fb8aa3b, v2
	v_exp_f32_e32 v2, v2
	v_pk_mul_f32 v[8:9], v[8:9], 0.5 op_sel_hi:[1,0]
	v_add_f32_e32 v2, 1.0, v2
	v_rcp_f32_e32 v15, v2
	v_mul_f32_e32 v2, 0x3d372713, v10
	v_mul_f32_e32 v2, v10, v2
	v_fma_f32 v2, v10, v2, v10
	v_mul_f32_e32 v2, 0x3f4c422a, v2
	v_add_f32_e32 v2, v2, v2
	v_mul_f32_e32 v2, 0x3fb8aa3b, v2
	v_exp_f32_e32 v2, v2
	v_pk_fma_f32 v[14:15], v[14:15], 2.0, 1.0 op_sel_hi:[1,0,0] neg_lo:[1,0,0] neg_hi:[1,0,0]
	v_add_f32_e32 v2, 1.0, v2
	v_pk_add_f32 v[14:15], v[14:15], 1.0 op_sel_hi:[1,0]
	s_nop 0
	v_pk_mul_f32 v[8:9], v[8:9], v[14:15]
	v_rcp_f32_e32 v14, v2
	v_mul_f32_e32 v2, 0x3d372713, v11
	v_mul_f32_e32 v2, v11, v2
	v_fma_f32 v2, v11, v2, v11
	v_mul_f32_e32 v2, 0x3f4c422a, v2
	v_add_f32_e32 v2, v2, v2
	v_mul_f32_e32 v2, 0x3fb8aa3b, v2
	v_exp_f32_e32 v2, v2
	v_pk_mul_f32 v[10:11], v[10:11], 0.5 op_sel_hi:[1,0]
	v_cvt_pk_f16_f32 v8, v8, v9
	v_add_f32_e32 v2, 1.0, v2
	v_rcp_f32_e32 v15, v2
	v_mul_f32_e32 v2, 0x3d372713, v4
	v_mul_f32_e32 v2, v4, v2
	v_fma_f32 v2, v4, v2, v4
	v_mul_f32_e32 v2, 0x3f4c422a, v2
	v_add_f32_e32 v2, v2, v2
	v_mul_f32_e32 v2, 0x3fb8aa3b, v2
	v_pk_fma_f32 v[14:15], v[14:15], 2.0, 1.0 op_sel_hi:[1,0,0] neg_lo:[1,0,0] neg_hi:[1,0,0]
	v_exp_f32_e32 v2, v2
	v_pk_add_f32 v[14:15], v[14:15], 1.0 op_sel_hi:[1,0]
	v_add_f32_e32 v2, 1.0, v2
	v_pk_mul_f32 v[10:11], v[10:11], v[14:15]
	s_nop 0
	v_cvt_pk_f16_f32 v9, v10, v11
	v_lshlrev_b64 v[10:11], 11, v[12:13]
	v_lshl_add_u64 v[10:11], v[68:69], 0, v[10:11]
	global_store_dwordx2 v[10:11], v[8:9], off
	v_rcp_f32_e32 v10, v2
	v_mul_f32_e32 v2, 0x3d372713, v5
	v_mul_f32_e32 v2, v5, v2
	v_fma_f32 v2, v5, v2, v5
	v_mul_f32_e32 v2, 0x3f4c422a, v2
	v_add_f32_e32 v2, v2, v2
	v_mul_f32_e32 v2, 0x3fb8aa3b, v2
	v_exp_f32_e32 v2, v2
	v_pk_mul_f32 v[4:5], v[4:5], 0.5 op_sel_hi:[1,0]
	v_lshl_add_u64 v[8:9], s[16:17], 0, v[64:65]
	v_add_f32_e32 v2, 1.0, v2
	v_rcp_f32_e32 v11, v2
	v_mul_f32_e32 v2, 0x3d372713, v6
	v_mul_f32_e32 v2, v6, v2
	v_fma_f32 v2, v6, v2, v6
	v_mul_f32_e32 v2, 0x3f4c422a, v2
	v_add_f32_e32 v2, v2, v2
	v_mul_f32_e32 v2, 0x3fb8aa3b, v2
	v_exp_f32_e32 v2, v2
	v_pk_fma_f32 v[10:11], v[10:11], 2.0, 1.0 op_sel_hi:[1,0,0] neg_lo:[1,0,0] neg_hi:[1,0,0]
	v_add_f32_e32 v2, 1.0, v2
	v_pk_add_f32 v[10:11], v[10:11], 1.0 op_sel_hi:[1,0]
	s_nop 0
	v_pk_mul_f32 v[4:5], v[4:5], v[10:11]
	v_rcp_f32_e32 v10, v2
	v_mul_f32_e32 v2, 0x3d372713, v7
	v_mul_f32_e32 v2, v7, v2
	v_fma_f32 v2, v7, v2, v7
	v_mul_f32_e32 v2, 0x3f4c422a, v2
	v_add_f32_e32 v2, v2, v2
	v_mul_f32_e32 v2, 0x3fb8aa3b, v2
	v_exp_f32_e32 v2, v2
	v_pk_mul_f32 v[6:7], v[6:7], 0.5 op_sel_hi:[1,0]
	v_cvt_pk_f16_f32 v4, v4, v5
	v_add_f32_e32 v2, 1.0, v2
	v_rcp_f32_e32 v11, v2
	s_nop 0
	v_pk_fma_f32 v[10:11], v[10:11], 2.0, 1.0 op_sel_hi:[1,0,0] neg_lo:[1,0,0] neg_hi:[1,0,0]
	s_nop 0
	v_pk_add_f32 v[10:11], v[10:11], 1.0 op_sel_hi:[1,0]
	s_nop 0
	v_pk_mul_f32 v[6:7], v[6:7], v[10:11]
	s_nop 0
	v_cvt_pk_f16_f32 v5, v6, v7
	v_lshlrev_b64 v[6:7], 11, v[8:9]
	v_lshl_add_u64 v[6:7], v[68:69], 0, v[6:7]
	global_store_dwordx2 v[6:7], v[4:5], off
	s_barrier
	s_cbranch_scc1 .LBB0_726
